# stack20 plus row-sum adds of P values that survive in registers through P.V moved from the VALU-bound QK/softmax section into the P.V section (second accumulator folded into the step sum)
# baseline (speedup 1.0000x reference)
; DI void finishSM(f32x16& p0, f32x16& p1, float alpha, float& l_reg, bf16x8& pa0, bf16x8& pa1, bf16x8& pa2, bf16x8& pa3) {
; #pragma unroll
;     for (int r = 0; r < 16; ++r) p1[r] = __builtin_amdgcn_exp2f(p1[r]);
;     float ps = 0;
; #pragma unroll
;     for (int r = 0; r < 16; ++r) ps += p0[r];
; #pragma unroll
;     for (int r = 0; r < 16; ++r) ps += p1[r];
;     { auto rr = __builtin_amdgcn_permlane32_swap(__float_as_uint(ps), __float_as_uint(ps), false, false); ps = __uint_as_float(rr[0]) + __uint_as_float(rr[1]); }
;     l_reg = l_reg * alpha + ps;
;     ...
;     AT_PK4(p0, 0, pa0); AT_PK4(p0, 8, pa1); AT_PK4(p1, 0, pa2); AT_PK4(p1, 8, pa3);
;     ...
; }
; DI void qkt(f32x16& p0, f32x16& p1, const char* Ks, const bf16x8* qr, const f32x16& negm, int r32, int hi) {
; #pragma unroll
;     for (int d0 = 0; d0 < 4; ++d0) { const int cb = (d0 * 16 + hi * 8) * 2;
;         const bf16x8 b0 = *reinterpret_cast<const bf16x8*>(Ks + AT_KSWZ(r32, cb));
;         const bf16x8 b1 = *reinterpret_cast<const bf16x8*>(Ks + AT_KSWZ(32 + r32, cb));
;         p0 = __builtin_amdgcn_mfma_f32_32x32x16_bf16(b0, qr[d0], d0 == 0 ? negm : p0, 0, 0, 0);
;         p1 = __builtin_amdgcn_mfma_f32_32x32x16_bf16(b1, qr[d0], d0 == 0 ? negm : p1, 0, 0, 0); }
; }
.LBB4_702:
	s_lshl_b32 s26, s66, 13
	s_add_i32 s26, s26, 0
	v_add_u32_e32 v72, s26, v205
	v_add_u32_e32 v112, s26, v206
	v_add_u32_e32 v180, s26, v207
	s_waitcnt lgkmcnt(1)
	v_mfma_f32_32x32x16_bf16 v[128:143], v[64:67], v[156:159], v[80:95]
	ds_read_b128 v[64:67], v72 offset:49152
	ds_read_b128 v[72:75], v72 offset:53248
	ds_read_b128 v[76:79], v112 offset:49152
	ds_read_b128 v[220:223], v112 offset:53248
	v_exp_f32_e32 v186, v97
	v_exp_f32_e32 v213, v98
	v_exp_f32_e32 v214, v99
	v_exp_f32_e32 v219, v100
	v_exp_f32_e32 v228, v101
	s_waitcnt lgkmcnt(4)
	v_mfma_f32_32x32x16_bf16 v[112:127], v[68:71], v[156:159], v[80:95]
	ds_read_b128 v[68:71], v180 offset:49152
	ds_read_b128 v[224:227], v180 offset:53248
	v_exp_f32_e32 v180, v96
	v_cvt_pk_bf16_f32 v96, v216, v218
	v_cvt_pk_bf16_f32 v97, v179, v217
	v_cvt_pk_bf16_f32 v98, v177, v215
	v_cvt_pk_bf16_f32 v99, v176, v178
	s_waitcnt lgkmcnt(4)
	v_mfma_f32_32x32x16_bf16 v[112:127], v[72:75], v[152:155], v[112:127]
	v_add_f32_e32 v75, 0, v216
	v_add_f32_e32 v75, v218, v75
	v_add_f32_e32 v75, v217, v75
	v_add_f32_e32 v75, v215, v75
	v_add_f32_e32 v75, v176, v75
	v_mfma_f32_32x32x16_bf16 v[128:143], v[64:67], v[152:155], v[128:143]
	v_add_f32_e32 v75, v172, v75
	s_waitcnt lgkmcnt(3)
	v_mfma_f32_32x32x16_bf16 v[128:143], v[76:79], v[148:151], v[128:143]
	v_add_f32_e32 v75, v180, v75
	v_add_f32_e32 v75, v186, v75
	v_exp_f32_e32 v64, v102
	v_exp_f32_e32 v65, v103
	v_exp_f32_e32 v66, v104
	s_waitcnt lgkmcnt(2)
	v_mfma_f32_32x32x16_bf16 v[112:127], v[220:223], v[148:151], v[112:127]
	v_exp_f32_e32 v67, v105
	v_exp_f32_e32 v105, v106
	v_exp_f32_e32 v106, v107
	v_exp_f32_e32 v107, v108
	v_exp_f32_e32 v72, v109
	v_exp_f32_e32 v73, v110
	v_exp_f32_e32 v74, v111
	s_waitcnt lgkmcnt(1)
	v_mfma_f32_32x32x16_bf16 v[128:143], v[68:71], v[144:147], v[128:143]
	v_add_f32_e32 v68, v213, v75
	v_add_f32_e32 v68, v214, v68
	v_add_f32_e32 v68, v219, v68
	v_add_f32_e32 v68, v228, v68
	v_add_f32_e32 v68, v64, v68
	v_add_f32_e32 v68, v65, v68
	v_add_f32_e32 v68, v66, v68
	v_add_f32_e32 v68, v67, v68
	s_waitcnt lgkmcnt(0)
	v_mfma_f32_32x32x16_bf16 v[112:127], v[224:227], v[144:147], v[112:127]
	v_add_f32_e32 v68, v105, v68
	v_add_f32_e32 v68, v106, v68
	v_add_f32_e32 v68, v107, v68
	v_add_f32_e32 v68, v72, v68
	v_add_f32_e32 v68, v73, v68
	v_add_f32_e32 v183, v74, v68
	v_cvt_pk_bf16_f32 v108, v173, v175
	v_cvt_pk_bf16_f32 v109, v171, v174
	v_cvt_pk_bf16_f32 v110, v169, v172
	v_cvt_pk_bf16_f32 v111, v168, v170
	v_cvt_pk_bf16_f32 v100, v180, v186
	v_cvt_pk_bf16_f32 v101, v213, v214
	v_cvt_pk_bf16_f32 v102, v219, v228
	v_cvt_pk_bf16_f32 v103, v64, v65
	v_cvt_pk_bf16_f32 v104, v66, v67
	v_cvt_pk_bf16_f32 v105, v105, v106
	v_cvt_pk_bf16_f32 v106, v107, v72
	v_cvt_pk_bf16_f32 v107, v73, v74
	s_add_u32 s74, s46, s28
	s_addc_u32 s75, s47, s29
	s_add_u32 s78, s74, 0x23808000
	s_addc_u32 s79, s75, 0
	s_add_u32 s80, s74, 0x2380a000
	s_addc_u32 s81, s75, 0
	s_add_u32 s76, s46, s30
	s_addc_u32 s77, s47, s31
	s_add_u32 s82, s76, 0x21804000
	s_addc_u32 s83, s77, 0
	s_lshl_b32 s92, s64, 14
	s_add_i32 s92, s92, s94
	s_mov_b32 m0, s92
	s_lshl_b32 s96, s64, 13
	global_load_lds_dwordx4 v249, s[78:79]
	s_addk_i32 s92, 0x400
	s_mov_b32 m0, s92
	s_add_i32 s96, s96, s95
	global_load_lds_dwordx4 v250, s[78:79]
	s_nop 0
	s_mov_b32 m0, s96
	s_nop 0
	global_load_lds_dwordx4 v251, s[82:83]
	s_andn2_b64 vcc, exec, s[2:3]
	s_cbranch_vccnz .LBB4_704
	s_mov_b64 s[2:3], s[8:9]
	global_store_dwordx2 v189, v[184:185], s[2:3] nt
; #define AT_SBAR() __builtin_amdgcn_sched_barrier(0)
; template <int OFF> DI s16x4 tr_read(int vb) { s16x4 r; asm volatile("ds_read_b64_tr_b16 %0, %1 offset:%2" : "=&v"(r) : "v"(vb), "i"(OFF) : "memory"); return r; }
; template <int D0> DI void pv_one(f32x16& od, int vb, bf16x8 pa0, bf16x8 pa1, bf16x8 pa2, bf16x8 pa3) {
;     const s16x4 l0 = tr_read<v_rd_off(D0, 0, 0)>(vb), h0 = tr_read<v_rd_off(D0, 0, 1)>(vb), l1 = tr_read<v_rd_off(D0, 1, 0)>(vb), h1 = tr_read<v_rd_off(D0, 1, 1)>(vb);
;     const s16x4 l2 = tr_read<v_rd_off(D0, 2, 0)>(vb), h2 = tr_read<v_rd_off(D0, 2, 1)>(vb), l3 = tr_read<v_rd_off(D0, 3, 0)>(vb), h3 = tr_read<v_rd_off(D0, 3, 1)>(vb);
;     asm volatile("s_waitcnt lgkmcnt(0)" ::: "memory"); AT_SBAR();
;     ...
;     od = __builtin_amdgcn_mfma_f32_32x32x16_bf16(AT_PK(l0, h0), pa0, od, 0, 0, 0);
;     od = __builtin_amdgcn_mfma_f32_32x32x16_bf16(AT_PK(l1, h1), pa1, od, 0, 0, 0);
;     od = __builtin_amdgcn_mfma_f32_32x32x16_bf16(AT_PK(l2, h2), pa2, od, 0, 0, 0);
;     od = __builtin_amdgcn_mfma_f32_32x32x16_bf16(AT_PK(l3, h3), pa3, od, 0, 0, 0);
;     ...
; }
; DI void pv_all_sm(f32x16* o, int vb, bf16x8 pa0, bf16x8 pa1, bf16x8 pa2, bf16x8 pa3, f32x16& p0, f32x16& p1, float& m_ref, f32x16& negm, float& alpha) {
;     pv_one<0>(o[0], vb, pa0, pa1, pa2, pa3);
;     float pmax = p0[0];
; #pragma unroll
;     for (int r = 1; r < 16; ++r) pmax = fmaxf(pmax, p0[r]);
;     pv_one<1>(o[1], vb, pa0, pa1, pa2, pa3);
; #pragma unroll
;     for (int r = 0; r < 16; ++r) pmax = fmaxf(pmax, p1[r]);
;     { auto rr = __builtin_amdgcn_permlane32_swap(__float_as_uint(pmax), __float_as_uint(pmax), false, false); pmax = fmaxf(__uint_as_float(rr[0]), __uint_as_float(rr[1])); }
;     pv_one<2>(o[2], vb, pa0, pa1, pa2, pa3);
;     alpha = 1.f;
;     if (__builtin_expect(!__all(pmax <= THRL), 0)) {
;         const float dl = fmaxf(pmax, 0.f); m_ref += dl; alpha = __builtin_amdgcn_exp2f(-dl);
; #pragma unroll
;         for (int r = 0; r < 16; ++r) { p0[r] -= dl; p1[r] -= dl; }
; #pragma unroll
;         for (int r = 0; r < 16; ++r) negm[r] = -m_ref;
;     }
;     pv_one<3>(o[3], vb, pa0, pa1, pa2, pa3);
; #pragma unroll
;     for (int r = 0; r < 16; ++r) p0[r] = __builtin_amdgcn_exp2f(p0[r]);
; }
.LBB4_704:
	s_lshl_b32 s67, s65, 14
	v_add_u32_e32 v186, s67, v253
	ds_read_b64_tr_b16 v[64:65], v186 offset:0
	ds_read_b64_tr_b16 v[66:67], v186 offset:0x100
	ds_read_b64_tr_b16 v[68:69], v186 offset:0x1000
	ds_read_b64_tr_b16 v[70:71], v186 offset:0x1100
	ds_read_b64_tr_b16 v[72:73], v186 offset:0x2000
	ds_read_b64_tr_b16 v[74:75], v186 offset:0x2100
	ds_read_b64_tr_b16 v[76:77], v186 offset:0x3000
	ds_read_b64_tr_b16 v[78:79], v186 offset:0x3100
	s_waitcnt lgkmcnt(0)
	v_mfma_f32_32x32x16_bf16 v[32:47], v[64:67], v[96:99], v[32:47]
	v_max_f32_e32 v64, v128, v129
	v_max3_f32 v64, v64, v130, v131
	v_max3_f32 v64, v64, v132, v133
	v_max3_f32 v64, v64, v134, v135
	v_max3_f32 v64, v64, v136, v137
	v_mfma_f32_32x32x16_bf16 v[32:47], v[68:71], v[108:111], v[32:47]
	v_max3_f32 v64, v64, v138, v139
	v_max3_f32 v66, v64, v140, v141
	ds_read_b64_tr_b16 v[64:65], v186 offset:0x200
	v_max3_f32 v180, v66, v142, v143
	ds_read_b64_tr_b16 v[66:67], v186 offset:0x300
	ds_read_b64_tr_b16 v[68:69], v186 offset:0x1200
	ds_read_b64_tr_b16 v[70:71], v186 offset:0x1300
	v_mfma_f32_32x32x16_bf16 v[32:47], v[72:75], v[100:103], v[32:47]
	v_add_f32_e32 v254, v179, v177
	v_add_f32_e32 v254, v178, v254
	ds_read_b64_tr_b16 v[72:73], v186 offset:0x2200
	ds_read_b64_tr_b16 v[74:75], v186 offset:0x2300
	ds_read_b64_tr_b16 v[214:215], v186 offset:0x3200
	ds_read_b64_tr_b16 v[216:217], v186 offset:0x3300
	v_mfma_f32_32x32x16_bf16 v[32:47], v[76:79], v[104:107], v[32:47]
	v_add_f32_e32 v254, v173, v254
	v_add_f32_e32 v254, v175, v254
	s_waitcnt lgkmcnt(0)
	v_mfma_f32_32x32x16_bf16 v[48:63], v[64:67], v[96:99], v[48:63]
	v_add_f32_e32 v254, v171, v254
	v_add_f32_e32 v254, v174, v254
	v_max3_f32 v76, v180, v112, v113
	v_max3_f32 v64, v76, v114, v115
	ds_read_b64_tr_b16 v[66:67], v186 offset:0x400
	v_max3_f32 v64, v64, v116, v117
	v_max3_f32 v64, v64, v118, v119
	v_max3_f32 v64, v64, v120, v121
	v_max3_f32 v64, v64, v122, v123
	v_mfma_f32_32x32x16_bf16 v[48:63], v[68:71], v[108:111], v[48:63]
	v_add_f32_e32 v254, v169, v254
	v_add_f32_e32 v254, v168, v254
	ds_read_b64_tr_b16 v[68:69], v186 offset:0x500
	ds_read_b64_tr_b16 v[70:71], v186 offset:0x1400
	v_max3_f32 v64, v64, v124, v125
	v_max3_f32 v64, v64, v126, v127
	v_mov_b32_e32 v65, v64
	s_nop 1
	v_permlane32_swap_b32_e32 v64, v65
	v_mfma_f32_32x32x16_bf16 v[48:63], v[72:75], v[100:103], v[48:63]
	ds_read_b64_tr_b16 v[72:73], v186 offset:0x1500
	ds_read_b64_tr_b16 v[74:75], v186 offset:0x2400
	ds_read_b64_tr_b16 v[76:77], v186 offset:0x2500
	ds_read_b64_tr_b16 v[218:219], v186 offset:0x3400
	ds_read_b64_tr_b16 v[220:221], v186 offset:0x3500
	v_mfma_f32_32x32x16_bf16 v[48:63], v[214:217], v[104:107], v[48:63]
	s_waitcnt lgkmcnt(0)
	v_max_f32_e32 v64, v64, v65
	v_mfma_f32_32x32x16_bf16 v[16:31], v[66:69], v[96:99], v[16:31]
	v_cmp_ge_f32_e32 vcc, s25, v64
	s_cmp_eq_u64 vcc, exec
	v_mfma_f32_32x32x16_bf16 v[16:31], v[70:73], v[108:111], v[16:31]
	v_mfma_f32_32x32x16_bf16 v[16:31], v[74:77], v[100:103], v[16:31]
	v_mfma_f32_32x32x16_bf16 v[16:31], v[218:221], v[104:107], v[16:31]
	s_cbranch_scc0 .LBB4_737
	v_mov_b32_e32 v180, 1.0
.LBB4_706:
	ds_read_b64_tr_b16 v[214:215], v186 offset:0x600
	ds_read_b64_tr_b16 v[216:217], v186 offset:0x700
	ds_read_b64_tr_b16 v[218:219], v186 offset:0x1600
	ds_read_b64_tr_b16 v[220:221], v186 offset:0x1700
	ds_read_b64_tr_b16 v[222:223], v186 offset:0x2600
	ds_read_b64_tr_b16 v[224:225], v186 offset:0x2700
	ds_read_b64_tr_b16 v[226:227], v186 offset:0x3600
	ds_read_b64_tr_b16 v[228:229], v186 offset:0x3700
	s_waitcnt lgkmcnt(0)
	v_mfma_f32_32x32x16_bf16 v[0:15], v[214:217], v[96:99], v[0:15]
	s_lshl_b32 s2, s64, 14
	s_lshl_b32 s3, s64, 13
	s_sub_i32 s78, s2, s3
	s_waitcnt vmcnt(3)
	v_mfma_f32_32x32x16_bf16 v[0:15], v[218:221], v[108:111], v[0:15]
	s_andn2_b64 s[2:3], exec, s[34:35]
	s_andn2_b64 vcc, exec, s[34:35]
	v_mfma_f32_32x32x16_bf16 v[0:15], v[222:225], v[100:103], v[0:15]
	v_mfma_f32_32x32x16_bf16 v[0:15], v[226:229], v[104:107], v[0:15]
	v_add_f32_e32 v254, v170, v254
	v_add_f32_e32 v183, v254, v183
	s_cbranch_vccnz .LBB4_711
	v_med3_f32 v97, v160, -v255, v255
	v_med3_f32 v98, v164, -v255, v255
	v_cvt_scalef32_pk_fp8_f32 v99, v97, v98, s93
	v_med3_f32 v97, v161, -v255, v255
	v_med3_f32 v98, v165, -v255, v255
	v_cvt_scalef32_pk_fp8_f32 v100, v97, v98, s93
	v_med3_f32 v97, v162, -v255, v255
	v_med3_f32 v98, v166, -v255, v255
	s_bitcmp1_b32 s58, 0
	v_cvt_scalef32_pk_fp8_f32 v101, v97, v98, s93
	s_cselect_b32 s8, 0x1100, 0
	v_med3_f32 v97, v163, -v255, v255
	v_med3_f32 v98, v167, -v255, v255
	v_cmp_eq_u32_e32 vcc, 0, v181
	v_add_u32_e32 v96, s8, v191
	v_cvt_scalef32_pk_fp8_f32 v102, v97, v98, s93
	s_and_b64 vcc, exec, vcc
	s_and_b32 s34, s58, 31
	ds_write_b16 v96, v99
	ds_write_b16 v96, v100 offset:68
	ds_write_b16 v96, v101 offset:136
	ds_write_b16 v96, v102 offset:204
	s_cbranch_vccnz .LBB4_735
	s_lshl_b32 s8, s34, 7
	s_lshl_b32 s9, s58, 6
	s_and_b32 s8, s8, 0xf00
	s_and_b32 s9, s9, 64
	s_or_b32 s26, s8, s9
	s_cbranch_execnz .LBB4_710

; DI void finishSM(f32x16& p0, f32x16& p1, float alpha, float& l_reg, bf16x8& pa0, bf16x8& pa1, bf16x8& pa2, bf16x8& pa3) {
; #pragma unroll
;     for (int r = 0; r < 16; ++r) p1[r] = __builtin_amdgcn_exp2f(p1[r]);
;     float ps = 0;
; #pragma unroll
;     for (int r = 0; r < 16; ++r) ps += p0[r];
; #pragma unroll
;     for (int r = 0; r < 16; ++r) ps += p1[r];
;     { auto rr = __builtin_amdgcn_permlane32_swap(__float_as_uint(ps), __float_as_uint(ps), false, false); ps = __uint_as_float(rr[0]) + __uint_as_float(rr[1]); }
;     l_reg = l_reg * alpha + ps;
;     ...
;     AT_PK4(p0, 0, pa0); AT_PK4(p0, 8, pa1); AT_PK4(p1, 0, pa2); AT_PK4(p1, 8, pa3);
;     ...
; }
; DI void qkt(f32x16& p0, f32x16& p1, const char* Ks, const bf16x8* qr, const f32x16& negm, int r32, int hi) {
; #pragma unroll
;     for (int d0 = 0; d0 < 4; ++d0) { const int cb = (d0 * 16 + hi * 8) * 2;
;         const bf16x8 b0 = *reinterpret_cast<const bf16x8*>(Ks + AT_KSWZ(r32, cb));
;         const bf16x8 b1 = *reinterpret_cast<const bf16x8*>(Ks + AT_KSWZ(32 + r32, cb));
;         p0 = __builtin_amdgcn_mfma_f32_32x32x16_bf16(b0, qr[d0], d0 == 0 ? negm : p0, 0, 0, 0);
;         p1 = __builtin_amdgcn_mfma_f32_32x32x16_bf16(b1, qr[d0], d0 == 0 ? negm : p1, 0, 0, 0); }
; }
.LBB4_723:
	v_exp_f32_e32 v186, v128
	v_exp_f32_e32 v230, v129
	v_exp_f32_e32 v231, v130
	v_exp_f32_e32 v232, v131
	v_exp_f32_e32 v233, v132
	v_exp_f32_e32 v234, v133
	v_exp_f32_e32 v235, v134
	v_exp_f32_e32 v236, v135
	v_exp_f32_e32 v237, v136
	v_exp_f32_e32 v238, v137
	v_exp_f32_e32 v239, v138
	v_exp_f32_e32 v240, v139
	v_exp_f32_e32 v241, v140
	v_exp_f32_e32 v242, v141
	v_exp_f32_e32 v243, v142
	v_exp_f32_e32 v244, v143
	v_add_u32_e32 v101, s78, v205
	v_add_u32_e32 v102, s78, v206
	v_add_u32_e32 v103, s78, v207
	ds_read_b128 v[172:175], v101 offset:49152
	ds_read_b128 v[176:179], v101 offset:53248
	ds_read_b128 v[214:217], v102 offset:49152
	ds_read_b128 v[218:221], v102 offset:53248
	ds_read_b128 v[222:225], v103 offset:49152
	ds_read_b128 v[226:229], v103 offset:53248
	v_exp_f32_e32 v112, v112
	v_exp_f32_e32 v113, v113
	v_exp_f32_e32 v114, v114
	s_waitcnt lgkmcnt(7)
	v_mfma_f32_32x32x16_bf16 v[128:143], v[96:99], v[156:159], v[80:95]
	v_exp_f32_e32 v115, v115
	v_exp_f32_e32 v116, v116
	v_exp_f32_e32 v117, v117
	v_exp_f32_e32 v118, v118
	v_exp_f32_e32 v119, v119
	s_waitcnt lgkmcnt(6)
	v_mfma_f32_32x32x16_bf16 v[96:111], v[168:171], v[156:159], v[80:95]
	v_exp_f32_e32 v168, v120
	v_add_f32_e32 v120, 0, v186
	v_add_f32_e32 v120, v230, v120
	v_add_f32_e32 v120, v231, v120
	v_add_f32_e32 v120, v232, v120
	v_add_f32_e32 v120, v233, v120
	v_add_f32_e32 v120, v234, v120
	v_add_f32_e32 v120, v235, v120
	v_add_f32_e32 v120, v236, v120
	v_add_f32_e32 v120, v237, v120
	v_add_f32_e32 v120, v238, v120
	s_waitcnt lgkmcnt(5)
	v_mfma_f32_32x32x16_bf16 v[128:143], v[172:175], v[152:155], v[128:143]
	v_add_f32_e32 v120, v239, v120
	v_add_f32_e32 v120, v240, v120
	v_add_f32_e32 v120, v241, v120
	v_add_f32_e32 v120, v242, v120
	v_add_f32_e32 v120, v243, v120
	v_add_f32_e32 v120, v244, v120
	v_add_f32_e32 v120, v112, v120
	s_waitcnt lgkmcnt(4)
	v_mfma_f32_32x32x16_bf16 v[96:111], v[176:179], v[152:155], v[96:111]
	v_add_f32_e32 v120, v113, v120
	v_add_f32_e32 v120, v114, v120
	v_add_f32_e32 v120, v115, v120
	v_add_f32_e32 v120, v116, v120
	v_exp_f32_e32 v169, v121
	v_add_f32_e32 v120, v117, v120
	v_exp_f32_e32 v170, v122
	s_waitcnt lgkmcnt(3)
	v_mfma_f32_32x32x16_bf16 v[128:143], v[214:217], v[148:151], v[128:143]
	v_add_f32_e32 v120, v118, v120
	v_exp_f32_e32 v171, v123
	v_add_f32_e32 v120, v119, v120
	v_exp_f32_e32 v172, v124
	v_exp_f32_e32 v173, v125
	s_waitcnt lgkmcnt(2)
	v_mfma_f32_32x32x16_bf16 v[96:111], v[218:221], v[148:151], v[96:111]
	v_exp_f32_e32 v174, v126
	v_exp_f32_e32 v175, v127
	v_add_f32_e32 v120, v174, v120
	s_waitcnt lgkmcnt(1)
	v_mfma_f32_32x32x16_bf16 v[128:143], v[222:225], v[144:147], v[128:143]
	v_add_f32_e32 v213, v175, v120
	v_cvt_pk_bf16_f32 v120, v186, v230
	v_cvt_pk_bf16_f32 v121, v231, v232
	v_cvt_pk_bf16_f32 v122, v233, v234
	v_cvt_pk_bf16_f32 v123, v235, v236
	v_cvt_pk_bf16_f32 v124, v237, v238
	s_waitcnt lgkmcnt(0)
	v_mfma_f32_32x32x16_bf16 v[96:111], v[226:229], v[144:147], v[96:111]
	v_cvt_pk_bf16_f32 v125, v239, v240
	v_cvt_pk_bf16_f32 v126, v241, v242
	v_cvt_pk_bf16_f32 v127, v243, v244
	v_cvt_pk_bf16_f32 v112, v112, v113
	v_cvt_pk_bf16_f32 v113, v114, v115
	v_cvt_pk_bf16_f32 v114, v116, v117
	v_cvt_pk_bf16_f32 v115, v118, v119
	v_cvt_pk_bf16_f32 v116, v168, v169
	v_cvt_pk_bf16_f32 v117, v170, v171
	v_cvt_pk_bf16_f32 v118, v172, v173
	v_cvt_pk_bf16_f32 v119, v174, v175
	s_add_u32 s78, s74, 0x2380c000
	s_addc_u32 s79, s75, 0
	s_add_u32 s74, s74, 0x2380e000
	s_addc_u32 s75, s75, 0
	s_add_u32 s76, s76, 0x21806000
	s_addc_u32 s77, s77, 0
	s_lshl_b32 s92, s65, 14
	s_add_i32 s92, s92, s94
	s_mov_b32 m0, s92
	s_lshl_b32 s96, s65, 13
	global_load_lds_dwordx4 v249, s[78:79]
	s_addk_i32 s92, 0x400
	s_mov_b32 m0, s92
	s_add_i32 s96, s96, s95
	global_load_lds_dwordx4 v250, s[78:79]
	s_nop 0
	s_mov_b32 m0, s96
	s_nop 0
	global_load_lds_dwordx4 v251, s[76:77]
	s_nop 0
	s_and_b64 vcc, exec, s[2:3]
	s_cbranch_vccnz .LBB4_725
	s_mov_b64 s[2:3], s[8:9]
	global_store_dwordx2 v189, v[184:185], s[2:3] nt
; #define AT_SBAR() __builtin_amdgcn_sched_barrier(0)
; template <int OFF> DI s16x4 tr_read(int vb) { s16x4 r; asm volatile("ds_read_b64_tr_b16 %0, %1 offset:%2" : "=&v"(r) : "v"(vb), "i"(OFF) : "memory"); return r; }
; template <int D0> DI void pv_one(f32x16& od, int vb, bf16x8 pa0, bf16x8 pa1, bf16x8 pa2, bf16x8 pa3) {
;     const s16x4 l0 = tr_read<v_rd_off(D0, 0, 0)>(vb), h0 = tr_read<v_rd_off(D0, 0, 1)>(vb), l1 = tr_read<v_rd_off(D0, 1, 0)>(vb), h1 = tr_read<v_rd_off(D0, 1, 1)>(vb);
;     const s16x4 l2 = tr_read<v_rd_off(D0, 2, 0)>(vb), h2 = tr_read<v_rd_off(D0, 2, 1)>(vb), l3 = tr_read<v_rd_off(D0, 3, 0)>(vb), h3 = tr_read<v_rd_off(D0, 3, 1)>(vb);
;     asm volatile("s_waitcnt lgkmcnt(0)" ::: "memory"); AT_SBAR();
;     ...
;     od = __builtin_amdgcn_mfma_f32_32x32x16_bf16(AT_PK(l0, h0), pa0, od, 0, 0, 0);
;     od = __builtin_amdgcn_mfma_f32_32x32x16_bf16(AT_PK(l1, h1), pa1, od, 0, 0, 0);
;     od = __builtin_amdgcn_mfma_f32_32x32x16_bf16(AT_PK(l2, h2), pa2, od, 0, 0, 0);
;     od = __builtin_amdgcn_mfma_f32_32x32x16_bf16(AT_PK(l3, h3), pa3, od, 0, 0, 0);
;     ...
; }
; DI void pv_all_sm(f32x16* o, int vb, bf16x8 pa0, bf16x8 pa1, bf16x8 pa2, bf16x8 pa3, f32x16& p0, f32x16& p1, float& m_ref, f32x16& negm, float& alpha) {
;     pv_one<0>(o[0], vb, pa0, pa1, pa2, pa3);
;     float pmax = p0[0];
; #pragma unroll
;     for (int r = 1; r < 16; ++r) pmax = fmaxf(pmax, p0[r]);
;     pv_one<1>(o[1], vb, pa0, pa1, pa2, pa3);
; #pragma unroll
;     for (int r = 0; r < 16; ++r) pmax = fmaxf(pmax, p1[r]);
;     { auto rr = __builtin_amdgcn_permlane32_swap(__float_as_uint(pmax), __float_as_uint(pmax), false, false); pmax = fmaxf(__uint_as_float(rr[0]), __uint_as_float(rr[1])); }
;     pv_one<2>(o[2], vb, pa0, pa1, pa2, pa3);
;     alpha = 1.f;
;     if (__builtin_expect(!__all(pmax <= THRL), 0)) {
;         const float dl = fmaxf(pmax, 0.f); m_ref += dl; alpha = __builtin_amdgcn_exp2f(-dl);
; #pragma unroll
;         for (int r = 0; r < 16; ++r) { p0[r] -= dl; p1[r] -= dl; }
; #pragma unroll
;         for (int r = 0; r < 16; ++r) negm[r] = -m_ref;
;     }
;     pv_one<3>(o[3], vb, pa0, pa1, pa2, pa3);
; #pragma unroll
;     for (int r = 0; r < 16; ++r) p0[r] = __builtin_amdgcn_exp2f(p0[r]);
; }
.LBB4_725:
	v_lshl_add_u32 v215, s66, 14, v253
	ds_read_b64_tr_b16 v[216:217], v215 offset:0
	ds_read_b64_tr_b16 v[218:219], v215 offset:0x100
	ds_read_b64_tr_b16 v[220:221], v215 offset:0x1000
	ds_read_b64_tr_b16 v[222:223], v215 offset:0x1100
	ds_read_b64_tr_b16 v[224:225], v215 offset:0x2000
	ds_read_b64_tr_b16 v[226:227], v215 offset:0x2100
	ds_read_b64_tr_b16 v[228:229], v215 offset:0x3000
	ds_read_b64_tr_b16 v[230:231], v215 offset:0x3100
	s_waitcnt lgkmcnt(0)
	v_mfma_f32_32x32x16_bf16 v[32:47], v[216:219], v[120:123], v[32:47]
	v_max_f32_e32 v186, v128, v129
	ds_read_b64_tr_b16 v[216:217], v215 offset:0x200
	ds_read_b64_tr_b16 v[218:219], v215 offset:0x300
	v_max3_f32 v186, v186, v130, v131
	v_max3_f32 v186, v186, v132, v133
	v_mfma_f32_32x32x16_bf16 v[32:47], v[220:223], v[124:127], v[32:47]
	ds_read_b64_tr_b16 v[220:221], v215 offset:0x1200
	ds_read_b64_tr_b16 v[222:223], v215 offset:0x1300
	v_max3_f32 v186, v186, v134, v135
	v_max3_f32 v186, v186, v136, v137
	v_max3_f32 v186, v186, v138, v139
	v_max3_f32 v186, v186, v140, v141
	v_max3_f32 v186, v186, v142, v143
	v_mfma_f32_32x32x16_bf16 v[32:47], v[224:227], v[112:115], v[32:47]
	v_add_f32_e32 v254, v168, v169
	v_add_f32_e32 v254, v170, v254
	ds_read_b64_tr_b16 v[224:225], v215 offset:0x2200
	ds_read_b64_tr_b16 v[226:227], v215 offset:0x2300
	ds_read_b64_tr_b16 v[232:233], v215 offset:0x3200
	ds_read_b64_tr_b16 v[234:235], v215 offset:0x3300
	v_mfma_f32_32x32x16_bf16 v[32:47], v[228:231], v[116:119], v[32:47]
	v_add_f32_e32 v254, v171, v254
	v_add_f32_e32 v254, v172, v254
	s_waitcnt lgkmcnt(0)
	v_mfma_f32_32x32x16_bf16 v[48:63], v[216:219], v[120:123], v[48:63]
	v_max3_f32 v186, v186, v96, v97
	v_max3_f32 v186, v186, v98, v99
	ds_read_b64_tr_b16 v[218:219], v215 offset:0x400
	v_max3_f32 v186, v186, v100, v101
	v_max3_f32 v186, v186, v102, v103
	v_max3_f32 v186, v186, v104, v105
	v_max3_f32 v186, v186, v106, v107
	v_mfma_f32_32x32x16_bf16 v[48:63], v[220:223], v[124:127], v[48:63]
	ds_read_b64_tr_b16 v[220:221], v215 offset:0x500
	ds_read_b64_tr_b16 v[222:223], v215 offset:0x1400
	v_max3_f32 v186, v186, v108, v109
	v_max3_f32 v186, v186, v110, v111
	v_mov_b32_e32 v216, v186
	s_nop 1
	v_permlane32_swap_b32_e32 v186, v216
	v_mfma_f32_32x32x16_bf16 v[48:63], v[224:227], v[112:115], v[48:63]
	ds_read_b64_tr_b16 v[224:225], v215 offset:0x1500
	ds_read_b64_tr_b16 v[226:227], v215 offset:0x2400
	ds_read_b64_tr_b16 v[228:229], v215 offset:0x2500
	ds_read_b64_tr_b16 v[236:237], v215 offset:0x3400
	ds_read_b64_tr_b16 v[238:239], v215 offset:0x3500
	v_mfma_f32_32x32x16_bf16 v[48:63], v[232:235], v[116:119], v[48:63]
	s_waitcnt lgkmcnt(0)
	v_max_f32_e32 v216, v186, v216
	v_mfma_f32_32x32x16_bf16 v[16:31], v[218:221], v[120:123], v[16:31]
	v_cmp_ge_f32_e32 vcc, s25, v216
	s_cmp_eq_u64 vcc, exec
	v_mov_b32_e32 v186, 1.0
	v_mfma_f32_32x32x16_bf16 v[16:31], v[222:225], v[124:127], v[16:31]
	v_mfma_f32_32x32x16_bf16 v[16:31], v[226:229], v[112:115], v[16:31]
	v_mfma_f32_32x32x16_bf16 v[16:31], v[236:239], v[116:119], v[16:31]
	s_cbranch_scc0 .LBB4_738
.LBB4_726:
	ds_read_b64_tr_b16 v[216:217], v215 offset:0x600
	ds_read_b64_tr_b16 v[218:219], v215 offset:0x700
	ds_read_b64_tr_b16 v[220:221], v215 offset:0x1600
	ds_read_b64_tr_b16 v[222:223], v215 offset:0x1700
	ds_read_b64_tr_b16 v[224:225], v215 offset:0x2600
	ds_read_b64_tr_b16 v[226:227], v215 offset:0x2700
	ds_read_b64_tr_b16 v[228:229], v215 offset:0x3600
	ds_read_b64_tr_b16 v[230:231], v215 offset:0x3700
	s_waitcnt lgkmcnt(0)
	v_mfma_f32_32x32x16_bf16 v[0:15], v[216:219], v[120:123], v[0:15]
	s_add_i32 s2, s67, 0
	s_waitcnt vmcnt(3)
	s_mov_b32 s26, 0
	s_andn2_b64 vcc, exec, s[34:35]
	v_mfma_f32_32x32x16_bf16 v[0:15], v[220:223], v[124:127], v[0:15]
	v_mfma_f32_32x32x16_bf16 v[0:15], v[224:227], v[112:115], v[0:15]
	s_andn2_b64 s[2:3], exec, s[34:35]
	v_mfma_f32_32x32x16_bf16 v[0:15], v[228:231], v[116:119], v[0:15]
	v_add_f32_e32 v254, v173, v254
	v_add_f32_e32 v213, v254, v213
	s_cbranch_vccnz .LBB4_731
	v_med3_f32 v113, v160, -v255, v255
	v_med3_f32 v114, v164, -v255, v255
	v_cvt_scalef32_pk_fp8_f32 v115, v113, v114, s93
	v_med3_f32 v113, v161, -v255, v255
	v_med3_f32 v114, v165, -v255, v255
	v_cvt_scalef32_pk_fp8_f32 v116, v113, v114, s93
	v_med3_f32 v113, v162, -v255, v255
	v_med3_f32 v114, v166, -v255, v255
	s_bitcmp1_b32 s58, 0
	v_cvt_scalef32_pk_fp8_f32 v117, v113, v114, s93
	s_cselect_b32 s8, 0x1100, 0
	v_med3_f32 v113, v163, -v255, v255
	v_med3_f32 v114, v167, -v255, v255
	v_cmp_eq_u32_e32 vcc, 0, v181
	v_add_u32_e32 v112, s8, v191
	v_cvt_scalef32_pk_fp8_f32 v118, v113, v114, s93
	s_and_b64 vcc, exec, vcc
	s_and_b32 s37, s58, 31
	ds_write_b16 v112, v115
	ds_write_b16 v112, v116 offset:68
	ds_write_b16 v112, v117 offset:136
	ds_write_b16 v112, v118 offset:204
	s_cbranch_vccnz .LBB4_736
	s_lshl_b32 s8, s37, 7
	s_lshl_b32 s9, s58, 6
	s_and_b32 s8, s8, 0xf00
	s_and_b32 s9, s9, 64
	s_or_b32 s26, s8, s9
	s_cbranch_execnz .LBB4_730

; DI void finishSM(f32x16& p0, f32x16& p1, float alpha, float& l_reg, bf16x8& pa0, bf16x8& pa1, bf16x8& pa2, bf16x8& pa3) {
; #pragma unroll
;     for (int r = 0; r < 16; ++r) p1[r] = __builtin_amdgcn_exp2f(p1[r]);
;     float ps = 0;
; #pragma unroll
;     for (int r = 0; r < 16; ++r) ps += p0[r];
; #pragma unroll
;     for (int r = 0; r < 16; ++r) ps += p1[r];
;     { auto rr = __builtin_amdgcn_permlane32_swap(__float_as_uint(ps), __float_as_uint(ps), false, false); ps = __uint_as_float(rr[0]) + __uint_as_float(rr[1]); }
;     l_reg = l_reg * alpha + ps;
;     ...
;     AT_PK4(p0, 0, pa0); AT_PK4(p0, 8, pa1); AT_PK4(p1, 0, pa2); AT_PK4(p1, 8, pa3);
;     ...
; }
; DI void qkt(f32x16& p0, f32x16& p1, const char* Ks, const bf16x8* qr, const f32x16& negm, int r32, int hi) {
; #pragma unroll
;     for (int d0 = 0; d0 < 4; ++d0) { const int cb = (d0 * 16 + hi * 8) * 2;
;         const bf16x8 b0 = *reinterpret_cast<const bf16x8*>(Ks + AT_KSWZ(r32, cb));
;         const bf16x8 b1 = *reinterpret_cast<const bf16x8*>(Ks + AT_KSWZ(32 + r32, cb));
;         p0 = __builtin_amdgcn_mfma_f32_32x32x16_bf16(b0, qr[d0], d0 == 0 ? negm : p0, 0, 0, 0);
;         p1 = __builtin_amdgcn_mfma_f32_32x32x16_bf16(b1, qr[d0], d0 == 0 ? negm : p1, 0, 0, 0); }
; }
.LBB4_775:
	s_lshl_b32 s20, s30, 13
	s_add_i32 s20, s20, 0
	v_add_u32_e32 v72, s20, v208
	v_add_u32_e32 v112, s20, v209
	v_add_u32_e32 v180, s20, v210
	s_waitcnt lgkmcnt(1)
	v_mfma_f32_32x32x16_bf16 v[128:143], v[64:67], v[156:159], v[80:95]
	ds_read_b128 v[64:67], v72 offset:49152
	ds_read_b128 v[72:75], v72 offset:53248
	ds_read_b128 v[76:79], v112 offset:49152
	ds_read_b128 v[224:227], v112 offset:53248
	v_exp_f32_e32 v182, v97
	v_exp_f32_e32 v217, v98
	v_exp_f32_e32 v218, v99
	v_exp_f32_e32 v223, v100
	v_exp_f32_e32 v232, v101
	s_waitcnt lgkmcnt(4)
	v_mfma_f32_32x32x16_bf16 v[112:127], v[68:71], v[156:159], v[80:95]
	ds_read_b128 v[68:71], v180 offset:49152
	ds_read_b128 v[228:231], v180 offset:53248
	v_exp_f32_e32 v180, v96
	v_cvt_pk_bf16_f32 v96, v220, v222
	v_cvt_pk_bf16_f32 v97, v179, v221
	v_cvt_pk_bf16_f32 v98, v177, v219
	v_cvt_pk_bf16_f32 v99, v176, v178
	s_waitcnt lgkmcnt(4)
	v_mfma_f32_32x32x16_bf16 v[112:127], v[72:75], v[152:155], v[112:127]
	v_add_f32_e32 v75, 0, v220
	v_add_f32_e32 v75, v222, v75
	v_add_f32_e32 v75, v221, v75
	v_add_f32_e32 v75, v219, v75
	v_add_f32_e32 v75, v176, v75
	v_mfma_f32_32x32x16_bf16 v[128:143], v[64:67], v[152:155], v[128:143]
	v_add_f32_e32 v75, v172, v75
	s_waitcnt lgkmcnt(3)
	v_mfma_f32_32x32x16_bf16 v[128:143], v[76:79], v[148:151], v[128:143]
	v_add_f32_e32 v75, v180, v75
	v_add_f32_e32 v75, v182, v75
	v_exp_f32_e32 v64, v102
	v_exp_f32_e32 v65, v103
	v_exp_f32_e32 v66, v104
	s_waitcnt lgkmcnt(2)
	v_mfma_f32_32x32x16_bf16 v[112:127], v[224:227], v[148:151], v[112:127]
	v_exp_f32_e32 v67, v105
	v_exp_f32_e32 v105, v106
	v_exp_f32_e32 v106, v107
	v_exp_f32_e32 v107, v108
	v_exp_f32_e32 v72, v109
	v_exp_f32_e32 v73, v110
	v_exp_f32_e32 v74, v111
	s_waitcnt lgkmcnt(1)
	v_mfma_f32_32x32x16_bf16 v[128:143], v[68:71], v[144:147], v[128:143]
	v_add_f32_e32 v68, v217, v75
	v_add_f32_e32 v68, v218, v68
	v_add_f32_e32 v68, v223, v68
	v_add_f32_e32 v68, v232, v68
	v_add_f32_e32 v68, v64, v68
	v_add_f32_e32 v68, v65, v68
	v_add_f32_e32 v68, v66, v68
	v_add_f32_e32 v68, v67, v68
	s_waitcnt lgkmcnt(0)
	v_mfma_f32_32x32x16_bf16 v[112:127], v[228:231], v[144:147], v[112:127]
	v_add_f32_e32 v68, v105, v68
	v_add_f32_e32 v68, v106, v68
	v_add_f32_e32 v68, v107, v68
	v_add_f32_e32 v68, v72, v68
	v_add_f32_e32 v68, v73, v68
	v_add_f32_e32 v215, v74, v68
	v_cvt_pk_bf16_f32 v108, v173, v175
	v_cvt_pk_bf16_f32 v109, v171, v174
	v_cvt_pk_bf16_f32 v110, v169, v172
	v_cvt_pk_bf16_f32 v111, v168, v170
	v_cvt_pk_bf16_f32 v100, v180, v182
	v_cvt_pk_bf16_f32 v101, v217, v218
	v_cvt_pk_bf16_f32 v102, v223, v232
	v_cvt_pk_bf16_f32 v103, v64, v65
	v_cvt_pk_bf16_f32 v104, v66, v67
	v_cvt_pk_bf16_f32 v105, v105, v106
	v_cvt_pk_bf16_f32 v106, v107, v72
	v_cvt_pk_bf16_f32 v107, v73, v74
	s_add_u32 s34, s46, s16
	s_addc_u32 s35, s47, s17
	s_add_u32 s24, s34, 0x23808000
	s_addc_u32 s25, s35, 0
	s_add_u32 s66, s34, 0x2380a000
	s_addc_u32 s67, s35, 0
	s_add_u32 s37, s46, s18
	s_addc_u32 s64, s47, s19
	s_add_u32 s74, s37, 0x21884000
	s_addc_u32 s75, s64, 0
	s_lshl_b32 s92, s15, 14
	s_add_i32 s92, s92, s94
	s_mov_b32 m0, s92
	s_lshl_b32 s96, s15, 13
	global_load_lds_dwordx4 v249, s[24:25]
	s_addk_i32 s92, 0x400
	s_mov_b32 m0, s92
	s_add_i32 s96, s96, s95
	global_load_lds_dwordx4 v250, s[24:25]
	s_nop 0
	s_mov_b32 m0, s96
	s_nop 0
	global_load_lds_dwordx4 v251, s[74:75]
	s_andn2_b64 vcc, exec, s[2:3]
	s_cbranch_vccnz .LBB4_777
	s_mov_b64 s[2:3], s[8:9]
	global_store_dwordx2 v193, v[184:185], s[2:3] nt
; #define AT_SBAR() __builtin_amdgcn_sched_barrier(0)
; template <int OFF> DI s16x4 tr_read(int vb) { s16x4 r; asm volatile("ds_read_b64_tr_b16 %0, %1 offset:%2" : "=&v"(r) : "v"(vb), "i"(OFF) : "memory"); return r; }
; template <int D0> DI void pv_one(f32x16& od, int vb, bf16x8 pa0, bf16x8 pa1, bf16x8 pa2, bf16x8 pa3) {
;     const s16x4 l0 = tr_read<v_rd_off(D0, 0, 0)>(vb), h0 = tr_read<v_rd_off(D0, 0, 1)>(vb), l1 = tr_read<v_rd_off(D0, 1, 0)>(vb), h1 = tr_read<v_rd_off(D0, 1, 1)>(vb);
;     const s16x4 l2 = tr_read<v_rd_off(D0, 2, 0)>(vb), h2 = tr_read<v_rd_off(D0, 2, 1)>(vb), l3 = tr_read<v_rd_off(D0, 3, 0)>(vb), h3 = tr_read<v_rd_off(D0, 3, 1)>(vb);
;     asm volatile("s_waitcnt lgkmcnt(0)" ::: "memory"); AT_SBAR();
;     ...
;     od = __builtin_amdgcn_mfma_f32_32x32x16_bf16(AT_PK(l0, h0), pa0, od, 0, 0, 0);
;     od = __builtin_amdgcn_mfma_f32_32x32x16_bf16(AT_PK(l1, h1), pa1, od, 0, 0, 0);
;     od = __builtin_amdgcn_mfma_f32_32x32x16_bf16(AT_PK(l2, h2), pa2, od, 0, 0, 0);
;     od = __builtin_amdgcn_mfma_f32_32x32x16_bf16(AT_PK(l3, h3), pa3, od, 0, 0, 0);
;     ...
; }
; DI void pv_all_sm(f32x16* o, int vb, bf16x8 pa0, bf16x8 pa1, bf16x8 pa2, bf16x8 pa3, f32x16& p0, f32x16& p1, float& m_ref, f32x16& negm, float& alpha) {
;     pv_one<0>(o[0], vb, pa0, pa1, pa2, pa3);
;     float pmax = p0[0];
; #pragma unroll
;     for (int r = 1; r < 16; ++r) pmax = fmaxf(pmax, p0[r]);
;     pv_one<1>(o[1], vb, pa0, pa1, pa2, pa3);
; #pragma unroll
;     for (int r = 0; r < 16; ++r) pmax = fmaxf(pmax, p1[r]);
;     { auto rr = __builtin_amdgcn_permlane32_swap(__float_as_uint(pmax), __float_as_uint(pmax), false, false); pmax = fmaxf(__uint_as_float(rr[0]), __uint_as_float(rr[1])); }
;     pv_one<2>(o[2], vb, pa0, pa1, pa2, pa3);
;     alpha = 1.f;
;     if (__builtin_expect(!__all(pmax <= THRL), 0)) {
;         const float dl = fmaxf(pmax, 0.f); m_ref += dl; alpha = __builtin_amdgcn_exp2f(-dl);
; #pragma unroll
;         for (int r = 0; r < 16; ++r) { p0[r] -= dl; p1[r] -= dl; }
; #pragma unroll
;         for (int r = 0; r < 16; ++r) negm[r] = -m_ref;
;     }
;     pv_one<3>(o[3], vb, pa0, pa1, pa2, pa3);
; #pragma unroll
;     for (int r = 0; r < 16; ++r) p0[r] = __builtin_amdgcn_exp2f(p0[r]);
; }
.LBB4_777:
	s_lshl_b32 s31, s29, 14
	v_add_u32_e32 v182, s31, v253
	ds_read_b64_tr_b16 v[64:65], v182 offset:0
	ds_read_b64_tr_b16 v[66:67], v182 offset:0x100
	ds_read_b64_tr_b16 v[68:69], v182 offset:0x1000
	ds_read_b64_tr_b16 v[70:71], v182 offset:0x1100
	ds_read_b64_tr_b16 v[72:73], v182 offset:0x2000
	ds_read_b64_tr_b16 v[74:75], v182 offset:0x2100
	ds_read_b64_tr_b16 v[76:77], v182 offset:0x3000
	ds_read_b64_tr_b16 v[78:79], v182 offset:0x3100
	s_waitcnt lgkmcnt(0)
	v_mfma_f32_32x32x16_bf16 v[48:63], v[64:67], v[96:99], v[48:63]
	v_max_f32_e32 v64, v128, v129
	v_max3_f32 v64, v64, v130, v131
	v_max3_f32 v64, v64, v132, v133
	v_max3_f32 v64, v64, v134, v135
	v_max3_f32 v64, v64, v136, v137
	v_mfma_f32_32x32x16_bf16 v[48:63], v[68:71], v[108:111], v[48:63]
	v_max3_f32 v64, v64, v138, v139
	v_max3_f32 v66, v64, v140, v141
	ds_read_b64_tr_b16 v[64:65], v182 offset:0x200
	v_max3_f32 v180, v66, v142, v143
	ds_read_b64_tr_b16 v[66:67], v182 offset:0x300
	ds_read_b64_tr_b16 v[68:69], v182 offset:0x1200
	ds_read_b64_tr_b16 v[70:71], v182 offset:0x1300
	v_mfma_f32_32x32x16_bf16 v[48:63], v[72:75], v[100:103], v[48:63]
	v_add_f32_e32 v254, v179, v177
	v_add_f32_e32 v254, v178, v254
	ds_read_b64_tr_b16 v[72:73], v182 offset:0x2200
	ds_read_b64_tr_b16 v[74:75], v182 offset:0x2300
	ds_read_b64_tr_b16 v[218:219], v182 offset:0x3200
	ds_read_b64_tr_b16 v[220:221], v182 offset:0x3300
	v_mfma_f32_32x32x16_bf16 v[48:63], v[76:79], v[104:107], v[48:63]
	v_add_f32_e32 v254, v173, v254
	v_add_f32_e32 v254, v175, v254
	s_waitcnt lgkmcnt(0)
	v_mfma_f32_32x32x16_bf16 v[32:47], v[64:67], v[96:99], v[32:47]
	v_add_f32_e32 v254, v171, v254
	v_add_f32_e32 v254, v174, v254
	v_max3_f32 v76, v180, v112, v113
	v_max3_f32 v64, v76, v114, v115
	ds_read_b64_tr_b16 v[66:67], v182 offset:0x400
	v_max3_f32 v64, v64, v116, v117
	v_max3_f32 v64, v64, v118, v119
	v_max3_f32 v64, v64, v120, v121
	v_max3_f32 v64, v64, v122, v123
	v_mfma_f32_32x32x16_bf16 v[32:47], v[68:71], v[108:111], v[32:47]
	v_add_f32_e32 v254, v169, v254
	v_add_f32_e32 v254, v168, v254
	ds_read_b64_tr_b16 v[68:69], v182 offset:0x500
	ds_read_b64_tr_b16 v[70:71], v182 offset:0x1400
	v_max3_f32 v64, v64, v124, v125
	v_max3_f32 v64, v64, v126, v127
	v_mov_b32_e32 v65, v64
	s_nop 1
	v_permlane32_swap_b32_e32 v64, v65
	v_mfma_f32_32x32x16_bf16 v[32:47], v[72:75], v[100:103], v[32:47]
	ds_read_b64_tr_b16 v[72:73], v182 offset:0x1500
	ds_read_b64_tr_b16 v[74:75], v182 offset:0x2400
	ds_read_b64_tr_b16 v[76:77], v182 offset:0x2500
	ds_read_b64_tr_b16 v[222:223], v182 offset:0x3400
	ds_read_b64_tr_b16 v[224:225], v182 offset:0x3500
	v_mfma_f32_32x32x16_bf16 v[32:47], v[218:221], v[104:107], v[32:47]
	s_waitcnt lgkmcnt(0)
	v_max_f32_e32 v64, v64, v65
	v_mfma_f32_32x32x16_bf16 v[16:31], v[66:69], v[96:99], v[16:31]
	v_cmp_ge_f32_e32 vcc, s26, v64
	s_cmp_eq_u64 vcc, exec
	v_mfma_f32_32x32x16_bf16 v[16:31], v[70:73], v[108:111], v[16:31]
	v_mfma_f32_32x32x16_bf16 v[16:31], v[74:77], v[100:103], v[16:31]
	v_mfma_f32_32x32x16_bf16 v[16:31], v[222:225], v[104:107], v[16:31]
	s_cbranch_scc0 .LBB4_810
	v_mov_b32_e32 v180, 1.0
.LBB4_779:
	ds_read_b64_tr_b16 v[218:219], v182 offset:0x600
	ds_read_b64_tr_b16 v[220:221], v182 offset:0x700
	ds_read_b64_tr_b16 v[222:223], v182 offset:0x1600
	ds_read_b64_tr_b16 v[224:225], v182 offset:0x1700
	ds_read_b64_tr_b16 v[226:227], v182 offset:0x2600
	ds_read_b64_tr_b16 v[228:229], v182 offset:0x2700
	ds_read_b64_tr_b16 v[230:231], v182 offset:0x3600
	ds_read_b64_tr_b16 v[232:233], v182 offset:0x3700
	s_waitcnt lgkmcnt(0)
	v_mfma_f32_32x32x16_bf16 v[0:15], v[218:221], v[96:99], v[0:15]
	s_lshl_b32 s2, s15, 14
	s_lshl_b32 s3, s15, 13
	s_sub_i32 s65, s2, s3
	s_waitcnt vmcnt(3)
	v_mfma_f32_32x32x16_bf16 v[0:15], v[222:225], v[108:111], v[0:15]
	s_andn2_b64 s[2:3], exec, s[22:23]
	s_andn2_b64 vcc, exec, s[22:23]
	v_mfma_f32_32x32x16_bf16 v[0:15], v[226:229], v[100:103], v[0:15]
	v_mfma_f32_32x32x16_bf16 v[0:15], v[230:233], v[104:107], v[0:15]
	v_add_f32_e32 v254, v170, v254
	v_add_f32_e32 v215, v254, v215
	s_cbranch_vccnz .LBB4_784
	v_med3_f32 v97, v160, -v255, v255
	v_med3_f32 v98, v164, -v255, v255
	v_cvt_scalef32_pk_fp8_f32 v99, v97, v98, s93
	v_med3_f32 v97, v161, -v255, v255
	v_med3_f32 v98, v165, -v255, v255
	v_cvt_scalef32_pk_fp8_f32 v100, v97, v98, s93
	v_med3_f32 v97, v162, -v255, v255
	v_med3_f32 v98, v166, -v255, v255
	s_bitcmp1_b32 s58, 0
	v_cvt_scalef32_pk_fp8_f32 v101, v97, v98, s93
	s_cselect_b32 s8, 0x1100, 0
	v_med3_f32 v97, v163, -v255, v255
	v_med3_f32 v98, v167, -v255, v255
	v_cmp_eq_u32_e32 vcc, 0, v181
	v_add_u32_e32 v96, s8, v195
	v_cvt_scalef32_pk_fp8_f32 v102, v97, v98, s93
	s_and_b64 vcc, exec, vcc
	s_and_b32 s22, s58, 31
	ds_write_b16 v96, v99
	ds_write_b16 v96, v100 offset:68
	ds_write_b16 v96, v101 offset:136
	ds_write_b16 v96, v102 offset:204
	s_cbranch_vccnz .LBB4_808
	s_lshl_b32 s8, s22, 7
	s_lshl_b32 s9, s58, 6
	s_and_b32 s8, s8, 0xf00
	s_and_b32 s9, s9, 64
	s_or_b32 s20, s8, s9
	s_cbranch_execnz .LBB4_783

; DI void finishSM(f32x16& p0, f32x16& p1, float alpha, float& l_reg, bf16x8& pa0, bf16x8& pa1, bf16x8& pa2, bf16x8& pa3) {
; #pragma unroll
;     for (int r = 0; r < 16; ++r) p1[r] = __builtin_amdgcn_exp2f(p1[r]);
;     float ps = 0;
; #pragma unroll
;     for (int r = 0; r < 16; ++r) ps += p0[r];
; #pragma unroll
;     for (int r = 0; r < 16; ++r) ps += p1[r];
;     { auto rr = __builtin_amdgcn_permlane32_swap(__float_as_uint(ps), __float_as_uint(ps), false, false); ps = __uint_as_float(rr[0]) + __uint_as_float(rr[1]); }
;     l_reg = l_reg * alpha + ps;
;     ...
;     AT_PK4(p0, 0, pa0); AT_PK4(p0, 8, pa1); AT_PK4(p1, 0, pa2); AT_PK4(p1, 8, pa3);
;     ...
; }
; DI void qkt(f32x16& p0, f32x16& p1, const char* Ks, const bf16x8* qr, const f32x16& negm, int r32, int hi) {
; #pragma unroll
;     for (int d0 = 0; d0 < 4; ++d0) { const int cb = (d0 * 16 + hi * 8) * 2;
;         const bf16x8 b0 = *reinterpret_cast<const bf16x8*>(Ks + AT_KSWZ(r32, cb));
;         const bf16x8 b1 = *reinterpret_cast<const bf16x8*>(Ks + AT_KSWZ(32 + r32, cb));
;         p0 = __builtin_amdgcn_mfma_f32_32x32x16_bf16(b0, qr[d0], d0 == 0 ? negm : p0, 0, 0, 0);
;         p1 = __builtin_amdgcn_mfma_f32_32x32x16_bf16(b1, qr[d0], d0 == 0 ? negm : p1, 0, 0, 0); }
; }
.LBB4_796:
	v_exp_f32_e32 v182, v128
	v_exp_f32_e32 v234, v129
	v_exp_f32_e32 v235, v130
	v_exp_f32_e32 v236, v131
	v_exp_f32_e32 v237, v132
	v_exp_f32_e32 v238, v133
	v_exp_f32_e32 v239, v134
	v_exp_f32_e32 v240, v135
	v_exp_f32_e32 v241, v136
	v_exp_f32_e32 v242, v137
	v_exp_f32_e32 v243, v138
	v_exp_f32_e32 v244, v139
	v_exp_f32_e32 v245, v140
	v_exp_f32_e32 v246, v141
	v_exp_f32_e32 v247, v142
	v_exp_f32_e32 v248, v143
	v_add_u32_e32 v101, s65, v208
	v_add_u32_e32 v102, s65, v209
	v_add_u32_e32 v103, s65, v210
	ds_read_b128 v[172:175], v101 offset:49152
	ds_read_b128 v[176:179], v101 offset:53248
	ds_read_b128 v[218:221], v102 offset:49152
	ds_read_b128 v[222:225], v102 offset:53248
	ds_read_b128 v[226:229], v103 offset:49152
	ds_read_b128 v[230:233], v103 offset:53248
	v_exp_f32_e32 v112, v112
	v_exp_f32_e32 v113, v113
	v_exp_f32_e32 v114, v114
	s_waitcnt lgkmcnt(7)
	v_mfma_f32_32x32x16_bf16 v[128:143], v[96:99], v[156:159], v[80:95]
	v_exp_f32_e32 v115, v115
	v_exp_f32_e32 v116, v116
	v_exp_f32_e32 v117, v117
	v_exp_f32_e32 v118, v118
	v_exp_f32_e32 v119, v119
	s_waitcnt lgkmcnt(6)
	v_mfma_f32_32x32x16_bf16 v[96:111], v[168:171], v[156:159], v[80:95]
	v_exp_f32_e32 v168, v120
	v_add_f32_e32 v120, 0, v182
	v_add_f32_e32 v120, v234, v120
	v_add_f32_e32 v120, v235, v120
	v_add_f32_e32 v120, v236, v120
	v_add_f32_e32 v120, v237, v120
	v_add_f32_e32 v120, v238, v120
	v_add_f32_e32 v120, v239, v120
	v_add_f32_e32 v120, v240, v120
	v_add_f32_e32 v120, v241, v120
	v_add_f32_e32 v120, v242, v120
	s_waitcnt lgkmcnt(5)
	v_mfma_f32_32x32x16_bf16 v[128:143], v[172:175], v[152:155], v[128:143]
	v_add_f32_e32 v120, v243, v120
	v_add_f32_e32 v120, v244, v120
	v_add_f32_e32 v120, v245, v120
	v_add_f32_e32 v120, v246, v120
	v_add_f32_e32 v120, v247, v120
	v_add_f32_e32 v120, v248, v120
	v_add_f32_e32 v120, v112, v120
	s_waitcnt lgkmcnt(4)
	v_mfma_f32_32x32x16_bf16 v[96:111], v[176:179], v[152:155], v[96:111]
	v_add_f32_e32 v120, v113, v120
	v_add_f32_e32 v120, v114, v120
	v_add_f32_e32 v120, v115, v120
	v_add_f32_e32 v120, v116, v120
	v_exp_f32_e32 v169, v121
	v_add_f32_e32 v120, v117, v120
	v_exp_f32_e32 v170, v122
	s_waitcnt lgkmcnt(3)
	v_mfma_f32_32x32x16_bf16 v[128:143], v[218:221], v[148:151], v[128:143]
	v_add_f32_e32 v120, v118, v120
	v_exp_f32_e32 v171, v123
	v_add_f32_e32 v120, v119, v120
	v_exp_f32_e32 v172, v124
	v_exp_f32_e32 v173, v125
	s_waitcnt lgkmcnt(2)
	v_mfma_f32_32x32x16_bf16 v[96:111], v[222:225], v[148:151], v[96:111]
	v_exp_f32_e32 v174, v126
	v_exp_f32_e32 v175, v127
	v_add_f32_e32 v120, v174, v120
	s_waitcnt lgkmcnt(1)
	v_mfma_f32_32x32x16_bf16 v[128:143], v[226:229], v[144:147], v[128:143]
	v_add_f32_e32 v217, v175, v120
	v_cvt_pk_bf16_f32 v120, v182, v234
	v_cvt_pk_bf16_f32 v121, v235, v236
	v_cvt_pk_bf16_f32 v122, v237, v238
	v_cvt_pk_bf16_f32 v123, v239, v240
	v_cvt_pk_bf16_f32 v124, v241, v242
	s_waitcnt lgkmcnt(0)
	v_mfma_f32_32x32x16_bf16 v[96:111], v[230:233], v[144:147], v[96:111]
	v_cvt_pk_bf16_f32 v125, v243, v244
	v_cvt_pk_bf16_f32 v126, v245, v246
	v_cvt_pk_bf16_f32 v127, v247, v248
	v_cvt_pk_bf16_f32 v112, v112, v113
	v_cvt_pk_bf16_f32 v113, v114, v115
	v_cvt_pk_bf16_f32 v114, v116, v117
	v_cvt_pk_bf16_f32 v115, v118, v119
	v_cvt_pk_bf16_f32 v116, v168, v169
	v_cvt_pk_bf16_f32 v117, v170, v171
	v_cvt_pk_bf16_f32 v118, v172, v173
	v_cvt_pk_bf16_f32 v119, v174, v175
	s_add_u32 s24, s34, 0x2380c000
	s_addc_u32 s25, s35, 0
	s_add_u32 s34, s34, 0x2380e000
	s_addc_u32 s35, s35, 0
	s_add_u32 s66, s37, 0x21886000
	s_addc_u32 s67, s64, 0
	s_lshl_b32 s92, s29, 14
	s_add_i32 s92, s92, s94
	s_mov_b32 m0, s92
	s_lshl_b32 s96, s29, 13
	global_load_lds_dwordx4 v249, s[24:25]
	s_addk_i32 s92, 0x400
	s_mov_b32 m0, s92
	s_add_i32 s96, s96, s95
	global_load_lds_dwordx4 v250, s[24:25]
	s_nop 0
	s_mov_b32 m0, s96
	s_nop 0
	global_load_lds_dwordx4 v251, s[66:67]
	s_nop 0
	s_and_b64 vcc, exec, s[2:3]
	s_cbranch_vccnz .LBB4_798
	s_mov_b64 s[2:3], s[8:9]
	global_store_dwordx2 v193, v[184:185], s[2:3] nt
; #define AT_SBAR() __builtin_amdgcn_sched_barrier(0)
; template <int OFF> DI s16x4 tr_read(int vb) { s16x4 r; asm volatile("ds_read_b64_tr_b16 %0, %1 offset:%2" : "=&v"(r) : "v"(vb), "i"(OFF) : "memory"); return r; }
; template <int D0> DI void pv_one(f32x16& od, int vb, bf16x8 pa0, bf16x8 pa1, bf16x8 pa2, bf16x8 pa3) {
;     const s16x4 l0 = tr_read<v_rd_off(D0, 0, 0)>(vb), h0 = tr_read<v_rd_off(D0, 0, 1)>(vb), l1 = tr_read<v_rd_off(D0, 1, 0)>(vb), h1 = tr_read<v_rd_off(D0, 1, 1)>(vb);
;     const s16x4 l2 = tr_read<v_rd_off(D0, 2, 0)>(vb), h2 = tr_read<v_rd_off(D0, 2, 1)>(vb), l3 = tr_read<v_rd_off(D0, 3, 0)>(vb), h3 = tr_read<v_rd_off(D0, 3, 1)>(vb);
;     asm volatile("s_waitcnt lgkmcnt(0)" ::: "memory"); AT_SBAR();
;     ...
;     od = __builtin_amdgcn_mfma_f32_32x32x16_bf16(AT_PK(l0, h0), pa0, od, 0, 0, 0);
;     od = __builtin_amdgcn_mfma_f32_32x32x16_bf16(AT_PK(l1, h1), pa1, od, 0, 0, 0);
;     od = __builtin_amdgcn_mfma_f32_32x32x16_bf16(AT_PK(l2, h2), pa2, od, 0, 0, 0);
;     od = __builtin_amdgcn_mfma_f32_32x32x16_bf16(AT_PK(l3, h3), pa3, od, 0, 0, 0);
;     ...
; }
; DI void pv_all_sm(f32x16* o, int vb, bf16x8 pa0, bf16x8 pa1, bf16x8 pa2, bf16x8 pa3, f32x16& p0, f32x16& p1, float& m_ref, f32x16& negm, float& alpha) {
;     pv_one<0>(o[0], vb, pa0, pa1, pa2, pa3);
;     float pmax = p0[0];
; #pragma unroll
;     for (int r = 1; r < 16; ++r) pmax = fmaxf(pmax, p0[r]);
;     pv_one<1>(o[1], vb, pa0, pa1, pa2, pa3);
; #pragma unroll
;     for (int r = 0; r < 16; ++r) pmax = fmaxf(pmax, p1[r]);
;     { auto rr = __builtin_amdgcn_permlane32_swap(__float_as_uint(pmax), __float_as_uint(pmax), false, false); pmax = fmaxf(__uint_as_float(rr[0]), __uint_as_float(rr[1])); }
;     pv_one<2>(o[2], vb, pa0, pa1, pa2, pa3);
;     alpha = 1.f;
;     if (__builtin_expect(!__all(pmax <= THRL), 0)) {
;         const float dl = fmaxf(pmax, 0.f); m_ref += dl; alpha = __builtin_amdgcn_exp2f(-dl);
; #pragma unroll
;         for (int r = 0; r < 16; ++r) { p0[r] -= dl; p1[r] -= dl; }
; #pragma unroll
;         for (int r = 0; r < 16; ++r) negm[r] = -m_ref;
;     }
;     pv_one<3>(o[3], vb, pa0, pa1, pa2, pa3);
; #pragma unroll
;     for (int r = 0; r < 16; ++r) p0[r] = __builtin_amdgcn_exp2f(p0[r]);
; }
.LBB4_798:
	v_lshl_add_u32 v219, s30, 14, v253
	ds_read_b64_tr_b16 v[220:221], v219 offset:0
	ds_read_b64_tr_b16 v[222:223], v219 offset:0x100
	ds_read_b64_tr_b16 v[224:225], v219 offset:0x1000
	ds_read_b64_tr_b16 v[226:227], v219 offset:0x1100
	ds_read_b64_tr_b16 v[228:229], v219 offset:0x2000
	ds_read_b64_tr_b16 v[230:231], v219 offset:0x2100
	ds_read_b64_tr_b16 v[232:233], v219 offset:0x3000
	ds_read_b64_tr_b16 v[234:235], v219 offset:0x3100
	s_waitcnt lgkmcnt(0)
	v_mfma_f32_32x32x16_bf16 v[48:63], v[220:223], v[120:123], v[48:63]
	v_max_f32_e32 v182, v128, v129
	ds_read_b64_tr_b16 v[220:221], v219 offset:0x200
	ds_read_b64_tr_b16 v[222:223], v219 offset:0x300
	v_max3_f32 v182, v182, v130, v131
	v_max3_f32 v182, v182, v132, v133
	v_mfma_f32_32x32x16_bf16 v[48:63], v[224:227], v[124:127], v[48:63]
	ds_read_b64_tr_b16 v[224:225], v219 offset:0x1200
	ds_read_b64_tr_b16 v[226:227], v219 offset:0x1300
	v_max3_f32 v182, v182, v134, v135
	v_max3_f32 v182, v182, v136, v137
	v_max3_f32 v182, v182, v138, v139
	v_max3_f32 v182, v182, v140, v141
	v_max3_f32 v182, v182, v142, v143
	v_mfma_f32_32x32x16_bf16 v[48:63], v[228:231], v[112:115], v[48:63]
	v_add_f32_e32 v254, v168, v169
	v_add_f32_e32 v254, v170, v254
	ds_read_b64_tr_b16 v[228:229], v219 offset:0x2200
	ds_read_b64_tr_b16 v[230:231], v219 offset:0x2300
	ds_read_b64_tr_b16 v[236:237], v219 offset:0x3200
	ds_read_b64_tr_b16 v[238:239], v219 offset:0x3300
	v_mfma_f32_32x32x16_bf16 v[48:63], v[232:235], v[116:119], v[48:63]
	v_add_f32_e32 v254, v171, v254
	v_add_f32_e32 v254, v172, v254
	s_waitcnt lgkmcnt(0)
	v_mfma_f32_32x32x16_bf16 v[32:47], v[220:223], v[120:123], v[32:47]
	v_max3_f32 v182, v182, v96, v97
	v_max3_f32 v182, v182, v98, v99
	ds_read_b64_tr_b16 v[222:223], v219 offset:0x400
	v_max3_f32 v182, v182, v100, v101
	v_max3_f32 v182, v182, v102, v103
	v_max3_f32 v182, v182, v104, v105
	v_max3_f32 v182, v182, v106, v107
	v_mfma_f32_32x32x16_bf16 v[32:47], v[224:227], v[124:127], v[32:47]
	ds_read_b64_tr_b16 v[224:225], v219 offset:0x500
	ds_read_b64_tr_b16 v[226:227], v219 offset:0x1400
	v_max3_f32 v182, v182, v108, v109
	v_max3_f32 v182, v182, v110, v111
	v_mov_b32_e32 v220, v182
	s_nop 1
	v_permlane32_swap_b32_e32 v182, v220
	v_mfma_f32_32x32x16_bf16 v[32:47], v[228:231], v[112:115], v[32:47]
	ds_read_b64_tr_b16 v[228:229], v219 offset:0x1500
	ds_read_b64_tr_b16 v[230:231], v219 offset:0x2400
	ds_read_b64_tr_b16 v[232:233], v219 offset:0x2500
	ds_read_b64_tr_b16 v[240:241], v219 offset:0x3400
	ds_read_b64_tr_b16 v[242:243], v219 offset:0x3500
	v_mfma_f32_32x32x16_bf16 v[32:47], v[236:239], v[116:119], v[32:47]
	s_waitcnt lgkmcnt(0)
	v_max_f32_e32 v220, v182, v220
	v_mfma_f32_32x32x16_bf16 v[16:31], v[222:225], v[120:123], v[16:31]
	v_cmp_ge_f32_e32 vcc, s26, v220
	s_cmp_eq_u64 vcc, exec
	v_mov_b32_e32 v182, 1.0
	v_mfma_f32_32x32x16_bf16 v[16:31], v[226:229], v[124:127], v[16:31]
	v_mfma_f32_32x32x16_bf16 v[16:31], v[230:233], v[112:115], v[16:31]
	v_mfma_f32_32x32x16_bf16 v[16:31], v[240:243], v[116:119], v[16:31]
	s_cbranch_scc0 .LBB4_811
.LBB4_799:
	ds_read_b64_tr_b16 v[220:221], v219 offset:0x600
	ds_read_b64_tr_b16 v[222:223], v219 offset:0x700
	ds_read_b64_tr_b16 v[224:225], v219 offset:0x1600
	ds_read_b64_tr_b16 v[226:227], v219 offset:0x1700
	ds_read_b64_tr_b16 v[228:229], v219 offset:0x2600
	ds_read_b64_tr_b16 v[230:231], v219 offset:0x2700
	ds_read_b64_tr_b16 v[232:233], v219 offset:0x3600
	ds_read_b64_tr_b16 v[234:235], v219 offset:0x3700
	s_waitcnt lgkmcnt(0)
	v_mfma_f32_32x32x16_bf16 v[0:15], v[220:223], v[120:123], v[0:15]
	s_add_i32 s2, s31, 0
	s_waitcnt vmcnt(3)
	s_mov_b32 s20, 0
	s_andn2_b64 vcc, exec, s[22:23]
	v_mfma_f32_32x32x16_bf16 v[0:15], v[224:227], v[124:127], v[0:15]
	v_mfma_f32_32x32x16_bf16 v[0:15], v[228:231], v[112:115], v[0:15]
	s_andn2_b64 s[2:3], exec, s[22:23]
	v_mfma_f32_32x32x16_bf16 v[0:15], v[232:235], v[116:119], v[0:15]
	v_add_f32_e32 v254, v173, v254
	v_add_f32_e32 v217, v254, v217
	s_cbranch_vccnz .LBB4_804
	v_med3_f32 v113, v160, -v255, v255
	v_med3_f32 v114, v164, -v255, v255
	v_cvt_scalef32_pk_fp8_f32 v115, v113, v114, s93
	v_med3_f32 v113, v161, -v255, v255
	v_med3_f32 v114, v165, -v255, v255
	v_cvt_scalef32_pk_fp8_f32 v116, v113, v114, s93
	v_med3_f32 v113, v162, -v255, v255
	v_med3_f32 v114, v166, -v255, v255
	s_bitcmp1_b32 s58, 0
	v_cvt_scalef32_pk_fp8_f32 v117, v113, v114, s93
	s_cselect_b32 s8, 0x1100, 0
	v_med3_f32 v113, v163, -v255, v255
	v_med3_f32 v114, v167, -v255, v255
	v_cmp_eq_u32_e32 vcc, 0, v181
	v_add_u32_e32 v112, s8, v195
	v_cvt_scalef32_pk_fp8_f32 v118, v113, v114, s93
	s_and_b64 vcc, exec, vcc
	s_and_b32 s24, s58, 31
	ds_write_b16 v112, v115
	ds_write_b16 v112, v116 offset:68
	ds_write_b16 v112, v117 offset:136
	ds_write_b16 v112, v118 offset:204
	s_cbranch_vccnz .LBB4_809
	s_lshl_b32 s8, s24, 7
	s_lshl_b32 s9, s58, 6
	s_and_b32 s8, s8, 0xf00
	s_and_b32 s9, s9, 64
	s_or_b32 s20, s8, s9
	s_cbranch_execnz .LBB4_803

; DI void finishSM(f32x16& p0, f32x16& p1, float alpha, float& l_reg, bf16x8& pa0, bf16x8& pa1, bf16x8& pa2, bf16x8& pa3) {
; #pragma unroll
;     for (int r = 0; r < 16; ++r) p1[r] = __builtin_amdgcn_exp2f(p1[r]);
;     float ps = 0;
; #pragma unroll
;     for (int r = 0; r < 16; ++r) ps += p0[r];
; #pragma unroll
;     for (int r = 0; r < 16; ++r) ps += p1[r];
;     { auto rr = __builtin_amdgcn_permlane32_swap(__float_as_uint(ps), __float_as_uint(ps), false, false); ps = __uint_as_float(rr[0]) + __uint_as_float(rr[1]); }
;     l_reg = l_reg * alpha + ps;
;     ...
;     AT_PK4(p0, 0, pa0); AT_PK4(p0, 8, pa1); AT_PK4(p1, 0, pa2); AT_PK4(p1, 8, pa3);
;     ...
; }
; DI void qkt(f32x16& p0, f32x16& p1, const char* Ks, const bf16x8* qr, const f32x16& negm, int r32, int hi) {
; #pragma unroll
;     for (int d0 = 0; d0 < 4; ++d0) { const int cb = (d0 * 16 + hi * 8) * 2;
;         const bf16x8 b0 = *reinterpret_cast<const bf16x8*>(Ks + AT_KSWZ(r32, cb));
;         const bf16x8 b1 = *reinterpret_cast<const bf16x8*>(Ks + AT_KSWZ(32 + r32, cb));
;         p0 = __builtin_amdgcn_mfma_f32_32x32x16_bf16(b0, qr[d0], d0 == 0 ? negm : p0, 0, 0, 0);
;         p1 = __builtin_amdgcn_mfma_f32_32x32x16_bf16(b1, qr[d0], d0 == 0 ? negm : p1, 0, 0, 0); }
; }
.LBB4_849:
	s_lshl_b32 s26, s64, 13
	s_add_i32 s26, s26, 0
	v_add_u32_e32 v72, s26, v204
	v_add_u32_e32 v112, s26, v205
	v_add_u32_e32 v180, s26, v206
	s_waitcnt lgkmcnt(1)
	v_mfma_f32_32x32x16_bf16 v[128:143], v[64:67], v[156:159], v[80:95]
	ds_read_b128 v[64:67], v72 offset:49152
	ds_read_b128 v[72:75], v72 offset:53248
	ds_read_b128 v[76:79], v112 offset:49152
	ds_read_b128 v[220:223], v112 offset:53248
	v_exp_f32_e32 v182, v97
	v_exp_f32_e32 v213, v98
	v_exp_f32_e32 v214, v99
	v_exp_f32_e32 v219, v100
	v_exp_f32_e32 v228, v101
	s_waitcnt lgkmcnt(4)
	v_mfma_f32_32x32x16_bf16 v[112:127], v[68:71], v[156:159], v[80:95]
	ds_read_b128 v[68:71], v180 offset:49152
	ds_read_b128 v[224:227], v180 offset:53248
	v_exp_f32_e32 v180, v96
	v_cvt_pk_bf16_f32 v96, v216, v218
	v_cvt_pk_bf16_f32 v97, v179, v217
	v_cvt_pk_bf16_f32 v98, v177, v215
	v_cvt_pk_bf16_f32 v99, v176, v178
	s_waitcnt lgkmcnt(4)
	v_mfma_f32_32x32x16_bf16 v[112:127], v[72:75], v[152:155], v[112:127]
	v_add_f32_e32 v75, 0, v216
	v_add_f32_e32 v75, v218, v75
	v_add_f32_e32 v75, v217, v75
	v_add_f32_e32 v75, v215, v75
	v_add_f32_e32 v75, v176, v75
	v_mfma_f32_32x32x16_bf16 v[128:143], v[64:67], v[152:155], v[128:143]
	v_add_f32_e32 v75, v172, v75
	s_waitcnt lgkmcnt(3)
	v_mfma_f32_32x32x16_bf16 v[128:143], v[76:79], v[148:151], v[128:143]
	v_add_f32_e32 v75, v180, v75
	v_add_f32_e32 v75, v182, v75
	v_exp_f32_e32 v64, v102
	v_exp_f32_e32 v65, v103
	v_exp_f32_e32 v66, v104
	s_waitcnt lgkmcnt(2)
	v_mfma_f32_32x32x16_bf16 v[112:127], v[220:223], v[148:151], v[112:127]
	v_exp_f32_e32 v67, v105
	v_exp_f32_e32 v105, v106
	v_exp_f32_e32 v106, v107
	v_exp_f32_e32 v107, v108
	v_exp_f32_e32 v72, v109
	v_exp_f32_e32 v73, v110
	v_exp_f32_e32 v74, v111
	s_waitcnt lgkmcnt(1)
	v_mfma_f32_32x32x16_bf16 v[128:143], v[68:71], v[144:147], v[128:143]
	v_add_f32_e32 v68, v213, v75
	v_add_f32_e32 v68, v214, v68
	v_add_f32_e32 v68, v219, v68
	v_add_f32_e32 v68, v228, v68
	v_add_f32_e32 v68, v64, v68
	v_add_f32_e32 v68, v65, v68
	v_add_f32_e32 v68, v66, v68
	v_add_f32_e32 v68, v67, v68
	s_waitcnt lgkmcnt(0)
	v_mfma_f32_32x32x16_bf16 v[112:127], v[224:227], v[144:147], v[112:127]
	v_add_f32_e32 v68, v105, v68
	v_add_f32_e32 v68, v106, v68
	v_add_f32_e32 v68, v107, v68
	v_add_f32_e32 v68, v72, v68
	v_add_f32_e32 v68, v73, v68
	v_add_f32_e32 v211, v74, v68
	v_cvt_pk_bf16_f32 v108, v173, v175
	v_cvt_pk_bf16_f32 v109, v171, v174
	v_cvt_pk_bf16_f32 v110, v169, v172
	v_cvt_pk_bf16_f32 v111, v168, v170
	v_cvt_pk_bf16_f32 v100, v180, v182
	v_cvt_pk_bf16_f32 v101, v213, v214
	v_cvt_pk_bf16_f32 v102, v219, v228
	v_cvt_pk_bf16_f32 v103, v64, v65
	v_cvt_pk_bf16_f32 v104, v66, v67
	v_cvt_pk_bf16_f32 v105, v105, v106
	v_cvt_pk_bf16_f32 v106, v107, v72
	v_cvt_pk_bf16_f32 v107, v73, v74
	s_add_u32 s66, s46, s28
	s_addc_u32 s67, s47, s29
	s_add_u32 s34, s66, 0x23808000
	s_addc_u32 s35, s67, 0
	s_add_u32 s76, s66, 0x2380a000
	s_addc_u32 s77, s67, 0
	s_add_u32 s74, s46, s24
	s_addc_u32 s75, s47, s25
	s_add_u32 s78, s74, 0x21804000
	s_addc_u32 s79, s75, 0
	s_lshl_b32 s92, s57, 14
	s_add_i32 s92, s92, s94
	s_mov_b32 m0, s92
	s_lshl_b32 s96, s57, 13
	global_load_lds_dwordx4 v249, s[34:35]
	s_addk_i32 s92, 0x400
	s_mov_b32 m0, s92
	s_add_i32 s96, s96, s95
	global_load_lds_dwordx4 v250, s[34:35]
	s_nop 0
	s_mov_b32 m0, s96
	s_nop 0
	global_load_lds_dwordx4 v251, s[78:79]
	s_andn2_b64 vcc, exec, s[2:3]
	s_cbranch_vccnz .LBB4_851
	s_mov_b64 s[2:3], s[8:9]
	global_store_dwordx2 v188, v[184:185], s[2:3] nt
; #define AT_SBAR() __builtin_amdgcn_sched_barrier(0)
; template <int OFF> DI s16x4 tr_read(int vb) { s16x4 r; asm volatile("ds_read_b64_tr_b16 %0, %1 offset:%2" : "=&v"(r) : "v"(vb), "i"(OFF) : "memory"); return r; }
; template <int D0> DI void pv_one(f32x16& od, int vb, bf16x8 pa0, bf16x8 pa1, bf16x8 pa2, bf16x8 pa3) {
;     const s16x4 l0 = tr_read<v_rd_off(D0, 0, 0)>(vb), h0 = tr_read<v_rd_off(D0, 0, 1)>(vb), l1 = tr_read<v_rd_off(D0, 1, 0)>(vb), h1 = tr_read<v_rd_off(D0, 1, 1)>(vb);
;     const s16x4 l2 = tr_read<v_rd_off(D0, 2, 0)>(vb), h2 = tr_read<v_rd_off(D0, 2, 1)>(vb), l3 = tr_read<v_rd_off(D0, 3, 0)>(vb), h3 = tr_read<v_rd_off(D0, 3, 1)>(vb);
;     asm volatile("s_waitcnt lgkmcnt(0)" ::: "memory"); AT_SBAR();
;     ...
;     od = __builtin_amdgcn_mfma_f32_32x32x16_bf16(AT_PK(l0, h0), pa0, od, 0, 0, 0);
;     od = __builtin_amdgcn_mfma_f32_32x32x16_bf16(AT_PK(l1, h1), pa1, od, 0, 0, 0);
;     od = __builtin_amdgcn_mfma_f32_32x32x16_bf16(AT_PK(l2, h2), pa2, od, 0, 0, 0);
;     od = __builtin_amdgcn_mfma_f32_32x32x16_bf16(AT_PK(l3, h3), pa3, od, 0, 0, 0);
;     ...
; }
; DI void pv_all_sm(f32x16* o, int vb, bf16x8 pa0, bf16x8 pa1, bf16x8 pa2, bf16x8 pa3, f32x16& p0, f32x16& p1, float& m_ref, f32x16& negm, float& alpha) {
;     pv_one<0>(o[0], vb, pa0, pa1, pa2, pa3);
;     float pmax = p0[0];
; #pragma unroll
;     for (int r = 1; r < 16; ++r) pmax = fmaxf(pmax, p0[r]);
;     pv_one<1>(o[1], vb, pa0, pa1, pa2, pa3);
; #pragma unroll
;     for (int r = 0; r < 16; ++r) pmax = fmaxf(pmax, p1[r]);
;     { auto rr = __builtin_amdgcn_permlane32_swap(__float_as_uint(pmax), __float_as_uint(pmax), false, false); pmax = fmaxf(__uint_as_float(rr[0]), __uint_as_float(rr[1])); }
;     pv_one<2>(o[2], vb, pa0, pa1, pa2, pa3);
;     alpha = 1.f;
;     if (__builtin_expect(!__all(pmax <= THRL), 0)) {
;         const float dl = fmaxf(pmax, 0.f); m_ref += dl; alpha = __builtin_amdgcn_exp2f(-dl);
; #pragma unroll
;         for (int r = 0; r < 16; ++r) { p0[r] -= dl; p1[r] -= dl; }
; #pragma unroll
;         for (int r = 0; r < 16; ++r) negm[r] = -m_ref;
;     }
;     pv_one<3>(o[3], vb, pa0, pa1, pa2, pa3);
; #pragma unroll
;     for (int r = 0; r < 16; ++r) p0[r] = __builtin_amdgcn_exp2f(p0[r]);
; }
.LBB4_851:
	s_lshl_b32 s65, s63, 14
	v_add_u32_e32 v182, s65, v253
	ds_read_b64_tr_b16 v[64:65], v182 offset:0
	ds_read_b64_tr_b16 v[66:67], v182 offset:0x100
	ds_read_b64_tr_b16 v[68:69], v182 offset:0x1000
	ds_read_b64_tr_b16 v[70:71], v182 offset:0x1100
	ds_read_b64_tr_b16 v[72:73], v182 offset:0x2000
	ds_read_b64_tr_b16 v[74:75], v182 offset:0x2100
	ds_read_b64_tr_b16 v[76:77], v182 offset:0x3000
	ds_read_b64_tr_b16 v[78:79], v182 offset:0x3100
	s_waitcnt lgkmcnt(0)
	v_mfma_f32_32x32x16_bf16 v[32:47], v[64:67], v[96:99], v[32:47]
	v_max_f32_e32 v64, v128, v129
	v_max3_f32 v64, v64, v130, v131
	v_max3_f32 v64, v64, v132, v133
	v_max3_f32 v64, v64, v134, v135
	v_max3_f32 v64, v64, v136, v137
	v_mfma_f32_32x32x16_bf16 v[32:47], v[68:71], v[108:111], v[32:47]
	v_max3_f32 v64, v64, v138, v139
	v_max3_f32 v66, v64, v140, v141
	ds_read_b64_tr_b16 v[64:65], v182 offset:0x200
	v_max3_f32 v180, v66, v142, v143
	ds_read_b64_tr_b16 v[66:67], v182 offset:0x300
	ds_read_b64_tr_b16 v[68:69], v182 offset:0x1200
	ds_read_b64_tr_b16 v[70:71], v182 offset:0x1300
	v_mfma_f32_32x32x16_bf16 v[32:47], v[72:75], v[100:103], v[32:47]
	v_add_f32_e32 v254, v179, v177
	v_add_f32_e32 v254, v178, v254
	ds_read_b64_tr_b16 v[72:73], v182 offset:0x2200
	ds_read_b64_tr_b16 v[74:75], v182 offset:0x2300
	ds_read_b64_tr_b16 v[214:215], v182 offset:0x3200
	ds_read_b64_tr_b16 v[216:217], v182 offset:0x3300
	v_mfma_f32_32x32x16_bf16 v[32:47], v[76:79], v[104:107], v[32:47]
	v_add_f32_e32 v254, v173, v254
	v_add_f32_e32 v254, v175, v254
	s_waitcnt lgkmcnt(0)
	v_mfma_f32_32x32x16_bf16 v[48:63], v[64:67], v[96:99], v[48:63]
	v_add_f32_e32 v254, v171, v254
	v_add_f32_e32 v254, v174, v254
	v_max3_f32 v76, v180, v112, v113
	v_max3_f32 v64, v76, v114, v115
	ds_read_b64_tr_b16 v[66:67], v182 offset:0x400
	v_max3_f32 v64, v64, v116, v117
	v_max3_f32 v64, v64, v118, v119
	v_max3_f32 v64, v64, v120, v121
	v_max3_f32 v64, v64, v122, v123
	v_mfma_f32_32x32x16_bf16 v[48:63], v[68:71], v[108:111], v[48:63]
	v_add_f32_e32 v254, v169, v254
	v_add_f32_e32 v254, v168, v254
	ds_read_b64_tr_b16 v[68:69], v182 offset:0x500
	ds_read_b64_tr_b16 v[70:71], v182 offset:0x1400
	v_max3_f32 v64, v64, v124, v125
	v_max3_f32 v64, v64, v126, v127
	v_mov_b32_e32 v65, v64
	s_nop 1
	v_permlane32_swap_b32_e32 v64, v65
	v_mfma_f32_32x32x16_bf16 v[48:63], v[72:75], v[100:103], v[48:63]
	ds_read_b64_tr_b16 v[72:73], v182 offset:0x1500
	ds_read_b64_tr_b16 v[74:75], v182 offset:0x2400
	ds_read_b64_tr_b16 v[76:77], v182 offset:0x2500
	ds_read_b64_tr_b16 v[218:219], v182 offset:0x3400
	ds_read_b64_tr_b16 v[220:221], v182 offset:0x3500
	v_mfma_f32_32x32x16_bf16 v[48:63], v[214:217], v[104:107], v[48:63]
	s_waitcnt lgkmcnt(0)
	v_max_f32_e32 v64, v64, v65
	v_mfma_f32_32x32x16_bf16 v[16:31], v[66:69], v[96:99], v[16:31]
	v_cmp_ge_f32_e32 vcc, s15, v64
	s_cmp_eq_u64 vcc, exec
	v_mfma_f32_32x32x16_bf16 v[16:31], v[70:73], v[108:111], v[16:31]
	v_mfma_f32_32x32x16_bf16 v[16:31], v[74:77], v[100:103], v[16:31]
	v_mfma_f32_32x32x16_bf16 v[16:31], v[218:221], v[104:107], v[16:31]
	s_cbranch_scc0 .LBB4_884
	v_mov_b32_e32 v180, 1.0
.LBB4_853:
	ds_read_b64_tr_b16 v[214:215], v182 offset:0x600
	ds_read_b64_tr_b16 v[216:217], v182 offset:0x700
	ds_read_b64_tr_b16 v[218:219], v182 offset:0x1600
	ds_read_b64_tr_b16 v[220:221], v182 offset:0x1700
	ds_read_b64_tr_b16 v[222:223], v182 offset:0x2600
	ds_read_b64_tr_b16 v[224:225], v182 offset:0x2700
	ds_read_b64_tr_b16 v[226:227], v182 offset:0x3600
	ds_read_b64_tr_b16 v[228:229], v182 offset:0x3700
	s_waitcnt lgkmcnt(0)
	v_mfma_f32_32x32x16_bf16 v[0:15], v[214:217], v[96:99], v[0:15]
	s_lshl_b32 s2, s57, 14
	s_lshl_b32 s3, s57, 13
	s_sub_i32 s76, s2, s3
	s_waitcnt vmcnt(3)
	v_mfma_f32_32x32x16_bf16 v[0:15], v[218:221], v[108:111], v[0:15]
	s_andn2_b64 s[2:3], exec, s[30:31]
	s_andn2_b64 vcc, exec, s[30:31]
	v_mfma_f32_32x32x16_bf16 v[0:15], v[222:225], v[100:103], v[0:15]
	v_mfma_f32_32x32x16_bf16 v[0:15], v[226:229], v[104:107], v[0:15]
	v_add_f32_e32 v254, v170, v254
	v_add_f32_e32 v211, v254, v211
	s_cbranch_vccnz .LBB4_858
	v_med3_f32 v97, v160, -v255, v255
	v_med3_f32 v98, v164, -v255, v255
	v_cvt_scalef32_pk_fp8_f32 v99, v97, v98, s93
	v_med3_f32 v97, v161, -v255, v255
	v_med3_f32 v98, v165, -v255, v255
	v_cvt_scalef32_pk_fp8_f32 v100, v97, v98, s93
	v_med3_f32 v97, v162, -v255, v255
	v_med3_f32 v98, v166, -v255, v255
	s_bitcmp1_b32 s58, 0
	v_cvt_scalef32_pk_fp8_f32 v101, v97, v98, s93
	s_cselect_b32 s8, 0x1100, 0
	v_med3_f32 v97, v163, -v255, v255
	v_med3_f32 v98, v167, -v255, v255
	v_cmp_eq_u32_e32 vcc, 0, v181
	v_add_u32_e32 v96, s8, v190
	v_cvt_scalef32_pk_fp8_f32 v102, v97, v98, s93
	s_and_b64 vcc, exec, vcc
	s_and_b32 s30, s58, 31
	ds_write_b16 v96, v99
	ds_write_b16 v96, v100 offset:68
	ds_write_b16 v96, v101 offset:136
	ds_write_b16 v96, v102 offset:204
	s_cbranch_vccnz .LBB4_882
	s_lshl_b32 s8, s30, 7
	s_lshl_b32 s9, s58, 6
	s_and_b32 s8, s8, 0xf00
	s_and_b32 s9, s9, 64
	s_or_b32 s26, s8, s9
	s_cbranch_execnz .LBB4_857

; DI void finishSM(f32x16& p0, f32x16& p1, float alpha, float& l_reg, bf16x8& pa0, bf16x8& pa1, bf16x8& pa2, bf16x8& pa3) {
; #pragma unroll
;     for (int r = 0; r < 16; ++r) p1[r] = __builtin_amdgcn_exp2f(p1[r]);
;     float ps = 0;
; #pragma unroll
;     for (int r = 0; r < 16; ++r) ps += p0[r];
; #pragma unroll
;     for (int r = 0; r < 16; ++r) ps += p1[r];
;     { auto rr = __builtin_amdgcn_permlane32_swap(__float_as_uint(ps), __float_as_uint(ps), false, false); ps = __uint_as_float(rr[0]) + __uint_as_float(rr[1]); }
;     l_reg = l_reg * alpha + ps;
;     ...
;     AT_PK4(p0, 0, pa0); AT_PK4(p0, 8, pa1); AT_PK4(p1, 0, pa2); AT_PK4(p1, 8, pa3);
;     ...
; }
; DI void qkt(f32x16& p0, f32x16& p1, const char* Ks, const bf16x8* qr, const f32x16& negm, int r32, int hi) {
; #pragma unroll
;     for (int d0 = 0; d0 < 4; ++d0) { const int cb = (d0 * 16 + hi * 8) * 2;
;         const bf16x8 b0 = *reinterpret_cast<const bf16x8*>(Ks + AT_KSWZ(r32, cb));
;         const bf16x8 b1 = *reinterpret_cast<const bf16x8*>(Ks + AT_KSWZ(32 + r32, cb));
;         p0 = __builtin_amdgcn_mfma_f32_32x32x16_bf16(b0, qr[d0], d0 == 0 ? negm : p0, 0, 0, 0);
;         p1 = __builtin_amdgcn_mfma_f32_32x32x16_bf16(b1, qr[d0], d0 == 0 ? negm : p1, 0, 0, 0); }
; }
.LBB4_870:
	v_exp_f32_e32 v182, v128
	v_exp_f32_e32 v230, v129
	v_exp_f32_e32 v231, v130
	v_exp_f32_e32 v232, v131
	v_exp_f32_e32 v233, v132
	v_exp_f32_e32 v234, v133
	v_exp_f32_e32 v235, v134
	v_exp_f32_e32 v236, v135
	v_exp_f32_e32 v237, v136
	v_exp_f32_e32 v238, v137
	v_exp_f32_e32 v239, v138
	v_exp_f32_e32 v240, v139
	v_exp_f32_e32 v241, v140
	v_exp_f32_e32 v242, v141
	v_exp_f32_e32 v243, v142
	v_exp_f32_e32 v244, v143
	v_add_u32_e32 v101, s76, v204
	v_add_u32_e32 v102, s76, v205
	v_add_u32_e32 v103, s76, v206
	ds_read_b128 v[172:175], v101 offset:49152
	ds_read_b128 v[176:179], v101 offset:53248
	ds_read_b128 v[214:217], v102 offset:49152
	ds_read_b128 v[218:221], v102 offset:53248
	ds_read_b128 v[222:225], v103 offset:49152
	ds_read_b128 v[226:229], v103 offset:53248
	v_exp_f32_e32 v112, v112
	v_exp_f32_e32 v113, v113
	v_exp_f32_e32 v114, v114
	s_waitcnt lgkmcnt(7)
	v_mfma_f32_32x32x16_bf16 v[128:143], v[96:99], v[156:159], v[80:95]
	v_exp_f32_e32 v115, v115
	v_exp_f32_e32 v116, v116
	v_exp_f32_e32 v117, v117
	v_exp_f32_e32 v118, v118
	v_exp_f32_e32 v119, v119
	s_waitcnt lgkmcnt(6)
	v_mfma_f32_32x32x16_bf16 v[96:111], v[168:171], v[156:159], v[80:95]
	v_exp_f32_e32 v168, v120
	v_add_f32_e32 v120, 0, v182
	v_add_f32_e32 v120, v230, v120
	v_add_f32_e32 v120, v231, v120
	v_add_f32_e32 v120, v232, v120
	v_add_f32_e32 v120, v233, v120
	v_add_f32_e32 v120, v234, v120
	v_add_f32_e32 v120, v235, v120
	v_add_f32_e32 v120, v236, v120
	v_add_f32_e32 v120, v237, v120
	v_add_f32_e32 v120, v238, v120
	s_waitcnt lgkmcnt(5)
	v_mfma_f32_32x32x16_bf16 v[128:143], v[172:175], v[152:155], v[128:143]
	v_add_f32_e32 v120, v239, v120
	v_add_f32_e32 v120, v240, v120
	v_add_f32_e32 v120, v241, v120
	v_add_f32_e32 v120, v242, v120
	v_add_f32_e32 v120, v243, v120
	v_add_f32_e32 v120, v244, v120
	v_add_f32_e32 v120, v112, v120
	s_waitcnt lgkmcnt(4)
	v_mfma_f32_32x32x16_bf16 v[96:111], v[176:179], v[152:155], v[96:111]
	v_add_f32_e32 v120, v113, v120
	v_add_f32_e32 v120, v114, v120
	v_add_f32_e32 v120, v115, v120
	v_add_f32_e32 v120, v116, v120
	v_exp_f32_e32 v169, v121
	v_add_f32_e32 v120, v117, v120
	v_exp_f32_e32 v170, v122
	s_waitcnt lgkmcnt(3)
	v_mfma_f32_32x32x16_bf16 v[128:143], v[214:217], v[148:151], v[128:143]
	v_add_f32_e32 v120, v118, v120
	v_exp_f32_e32 v171, v123
	v_add_f32_e32 v120, v119, v120
	v_exp_f32_e32 v172, v124
	v_exp_f32_e32 v173, v125
	s_waitcnt lgkmcnt(2)
	v_mfma_f32_32x32x16_bf16 v[96:111], v[218:221], v[148:151], v[96:111]
	v_exp_f32_e32 v174, v126
	v_exp_f32_e32 v175, v127
	v_add_f32_e32 v120, v174, v120
	s_waitcnt lgkmcnt(1)
	v_mfma_f32_32x32x16_bf16 v[128:143], v[222:225], v[144:147], v[128:143]
	v_add_f32_e32 v213, v175, v120
	v_cvt_pk_bf16_f32 v120, v182, v230
	v_cvt_pk_bf16_f32 v121, v231, v232
	v_cvt_pk_bf16_f32 v122, v233, v234
	v_cvt_pk_bf16_f32 v123, v235, v236
	v_cvt_pk_bf16_f32 v124, v237, v238
	s_waitcnt lgkmcnt(0)
	v_mfma_f32_32x32x16_bf16 v[96:111], v[226:229], v[144:147], v[96:111]
	v_cvt_pk_bf16_f32 v125, v239, v240
	v_cvt_pk_bf16_f32 v126, v241, v242
	v_cvt_pk_bf16_f32 v127, v243, v244
	v_cvt_pk_bf16_f32 v112, v112, v113
	v_cvt_pk_bf16_f32 v113, v114, v115
	v_cvt_pk_bf16_f32 v114, v116, v117
	v_cvt_pk_bf16_f32 v115, v118, v119
	v_cvt_pk_bf16_f32 v116, v168, v169
	v_cvt_pk_bf16_f32 v117, v170, v171
	v_cvt_pk_bf16_f32 v118, v172, v173
	v_cvt_pk_bf16_f32 v119, v174, v175
	s_add_u32 s34, s66, 0x2380c000
	s_addc_u32 s35, s67, 0
	s_add_u32 s66, s66, 0x2380e000
	s_addc_u32 s67, s67, 0
	s_add_u32 s74, s74, 0x21806000
	s_addc_u32 s75, s75, 0
	s_lshl_b32 s92, s63, 14
	s_add_i32 s92, s92, s94
	s_mov_b32 m0, s92
	s_lshl_b32 s96, s63, 13
	global_load_lds_dwordx4 v249, s[34:35]
	s_addk_i32 s92, 0x400
	s_mov_b32 m0, s92
	s_add_i32 s96, s96, s95
	global_load_lds_dwordx4 v250, s[34:35]
	s_nop 0
	s_mov_b32 m0, s96
	s_nop 0
	global_load_lds_dwordx4 v251, s[74:75]
	s_nop 0
	s_and_b64 vcc, exec, s[2:3]
	s_cbranch_vccnz .LBB4_872
	s_mov_b64 s[2:3], s[8:9]
	global_store_dwordx2 v188, v[184:185], s[2:3] nt
; #define AT_SBAR() __builtin_amdgcn_sched_barrier(0)
; template <int OFF> DI s16x4 tr_read(int vb) { s16x4 r; asm volatile("ds_read_b64_tr_b16 %0, %1 offset:%2" : "=&v"(r) : "v"(vb), "i"(OFF) : "memory"); return r; }
; template <int D0> DI void pv_one(f32x16& od, int vb, bf16x8 pa0, bf16x8 pa1, bf16x8 pa2, bf16x8 pa3) {
;     const s16x4 l0 = tr_read<v_rd_off(D0, 0, 0)>(vb), h0 = tr_read<v_rd_off(D0, 0, 1)>(vb), l1 = tr_read<v_rd_off(D0, 1, 0)>(vb), h1 = tr_read<v_rd_off(D0, 1, 1)>(vb);
;     const s16x4 l2 = tr_read<v_rd_off(D0, 2, 0)>(vb), h2 = tr_read<v_rd_off(D0, 2, 1)>(vb), l3 = tr_read<v_rd_off(D0, 3, 0)>(vb), h3 = tr_read<v_rd_off(D0, 3, 1)>(vb);
;     asm volatile("s_waitcnt lgkmcnt(0)" ::: "memory"); AT_SBAR();
;     ...
;     od = __builtin_amdgcn_mfma_f32_32x32x16_bf16(AT_PK(l0, h0), pa0, od, 0, 0, 0);
;     od = __builtin_amdgcn_mfma_f32_32x32x16_bf16(AT_PK(l1, h1), pa1, od, 0, 0, 0);
;     od = __builtin_amdgcn_mfma_f32_32x32x16_bf16(AT_PK(l2, h2), pa2, od, 0, 0, 0);
;     od = __builtin_amdgcn_mfma_f32_32x32x16_bf16(AT_PK(l3, h3), pa3, od, 0, 0, 0);
;     ...
; }
; DI void pv_all_sm(f32x16* o, int vb, bf16x8 pa0, bf16x8 pa1, bf16x8 pa2, bf16x8 pa3, f32x16& p0, f32x16& p1, float& m_ref, f32x16& negm, float& alpha) {
;     pv_one<0>(o[0], vb, pa0, pa1, pa2, pa3);
;     float pmax = p0[0];
; #pragma unroll
;     for (int r = 1; r < 16; ++r) pmax = fmaxf(pmax, p0[r]);
;     pv_one<1>(o[1], vb, pa0, pa1, pa2, pa3);
; #pragma unroll
;     for (int r = 0; r < 16; ++r) pmax = fmaxf(pmax, p1[r]);
;     { auto rr = __builtin_amdgcn_permlane32_swap(__float_as_uint(pmax), __float_as_uint(pmax), false, false); pmax = fmaxf(__uint_as_float(rr[0]), __uint_as_float(rr[1])); }
;     pv_one<2>(o[2], vb, pa0, pa1, pa2, pa3);
;     alpha = 1.f;
;     if (__builtin_expect(!__all(pmax <= THRL), 0)) {
;         const float dl = fmaxf(pmax, 0.f); m_ref += dl; alpha = __builtin_amdgcn_exp2f(-dl);
; #pragma unroll
;         for (int r = 0; r < 16; ++r) { p0[r] -= dl; p1[r] -= dl; }
; #pragma unroll
;         for (int r = 0; r < 16; ++r) negm[r] = -m_ref;
;     }
;     pv_one<3>(o[3], vb, pa0, pa1, pa2, pa3);
; #pragma unroll
;     for (int r = 0; r < 16; ++r) p0[r] = __builtin_amdgcn_exp2f(p0[r]);
; }
.LBB4_872:
	v_lshl_add_u32 v215, s64, 14, v253
	ds_read_b64_tr_b16 v[216:217], v215 offset:0
	ds_read_b64_tr_b16 v[218:219], v215 offset:0x100
	ds_read_b64_tr_b16 v[220:221], v215 offset:0x1000
	ds_read_b64_tr_b16 v[222:223], v215 offset:0x1100
	ds_read_b64_tr_b16 v[224:225], v215 offset:0x2000
	ds_read_b64_tr_b16 v[226:227], v215 offset:0x2100
	ds_read_b64_tr_b16 v[228:229], v215 offset:0x3000
	ds_read_b64_tr_b16 v[230:231], v215 offset:0x3100
	s_waitcnt lgkmcnt(0)
	v_mfma_f32_32x32x16_bf16 v[32:47], v[216:219], v[120:123], v[32:47]
	v_max_f32_e32 v182, v128, v129
	ds_read_b64_tr_b16 v[216:217], v215 offset:0x200
	ds_read_b64_tr_b16 v[218:219], v215 offset:0x300
	v_max3_f32 v182, v182, v130, v131
	v_max3_f32 v182, v182, v132, v133
	v_mfma_f32_32x32x16_bf16 v[32:47], v[220:223], v[124:127], v[32:47]
	ds_read_b64_tr_b16 v[220:221], v215 offset:0x1200
	ds_read_b64_tr_b16 v[222:223], v215 offset:0x1300
	v_max3_f32 v182, v182, v134, v135
	v_max3_f32 v182, v182, v136, v137
	v_max3_f32 v182, v182, v138, v139
	v_max3_f32 v182, v182, v140, v141
	v_max3_f32 v182, v182, v142, v143
	v_mfma_f32_32x32x16_bf16 v[32:47], v[224:227], v[112:115], v[32:47]
	v_add_f32_e32 v254, v168, v169
	v_add_f32_e32 v254, v170, v254
	ds_read_b64_tr_b16 v[224:225], v215 offset:0x2200
	ds_read_b64_tr_b16 v[226:227], v215 offset:0x2300
	ds_read_b64_tr_b16 v[232:233], v215 offset:0x3200
	ds_read_b64_tr_b16 v[234:235], v215 offset:0x3300
	v_mfma_f32_32x32x16_bf16 v[32:47], v[228:231], v[116:119], v[32:47]
	v_add_f32_e32 v254, v171, v254
	v_add_f32_e32 v254, v172, v254
	s_waitcnt lgkmcnt(0)
	v_mfma_f32_32x32x16_bf16 v[48:63], v[216:219], v[120:123], v[48:63]
	v_max3_f32 v182, v182, v96, v97
	v_max3_f32 v182, v182, v98, v99
	ds_read_b64_tr_b16 v[218:219], v215 offset:0x400
	v_max3_f32 v182, v182, v100, v101
	v_max3_f32 v182, v182, v102, v103
	v_max3_f32 v182, v182, v104, v105
	v_max3_f32 v182, v182, v106, v107
	v_mfma_f32_32x32x16_bf16 v[48:63], v[220:223], v[124:127], v[48:63]
	ds_read_b64_tr_b16 v[220:221], v215 offset:0x500
	ds_read_b64_tr_b16 v[222:223], v215 offset:0x1400
	v_max3_f32 v182, v182, v108, v109
	v_max3_f32 v182, v182, v110, v111
	v_mov_b32_e32 v216, v182
	s_nop 1
	v_permlane32_swap_b32_e32 v182, v216
	v_mfma_f32_32x32x16_bf16 v[48:63], v[224:227], v[112:115], v[48:63]
	ds_read_b64_tr_b16 v[224:225], v215 offset:0x1500
	ds_read_b64_tr_b16 v[226:227], v215 offset:0x2400
	ds_read_b64_tr_b16 v[228:229], v215 offset:0x2500
	ds_read_b64_tr_b16 v[236:237], v215 offset:0x3400
	ds_read_b64_tr_b16 v[238:239], v215 offset:0x3500
	v_mfma_f32_32x32x16_bf16 v[48:63], v[232:235], v[116:119], v[48:63]
	s_waitcnt lgkmcnt(0)
	v_max_f32_e32 v216, v182, v216
	v_mfma_f32_32x32x16_bf16 v[16:31], v[218:221], v[120:123], v[16:31]
	v_cmp_ge_f32_e32 vcc, s15, v216
	s_cmp_eq_u64 vcc, exec
	v_mov_b32_e32 v182, 1.0
	v_mfma_f32_32x32x16_bf16 v[16:31], v[222:225], v[124:127], v[16:31]
	v_mfma_f32_32x32x16_bf16 v[16:31], v[226:229], v[112:115], v[16:31]
	v_mfma_f32_32x32x16_bf16 v[16:31], v[236:239], v[116:119], v[16:31]
	s_cbranch_scc0 .LBB4_885
.LBB4_873:
	ds_read_b64_tr_b16 v[216:217], v215 offset:0x600
	ds_read_b64_tr_b16 v[218:219], v215 offset:0x700
	ds_read_b64_tr_b16 v[220:221], v215 offset:0x1600
	ds_read_b64_tr_b16 v[222:223], v215 offset:0x1700
	ds_read_b64_tr_b16 v[224:225], v215 offset:0x2600
	ds_read_b64_tr_b16 v[226:227], v215 offset:0x2700
	ds_read_b64_tr_b16 v[228:229], v215 offset:0x3600
	ds_read_b64_tr_b16 v[230:231], v215 offset:0x3700
	s_waitcnt lgkmcnt(0)
	v_mfma_f32_32x32x16_bf16 v[0:15], v[216:219], v[120:123], v[0:15]
	s_add_i32 s2, s65, 0
	s_waitcnt vmcnt(3)
	s_mov_b32 s26, 0
	s_andn2_b64 vcc, exec, s[30:31]
	v_mfma_f32_32x32x16_bf16 v[0:15], v[220:223], v[124:127], v[0:15]
	v_mfma_f32_32x32x16_bf16 v[0:15], v[224:227], v[112:115], v[0:15]
	s_andn2_b64 s[2:3], exec, s[30:31]
	v_mfma_f32_32x32x16_bf16 v[0:15], v[228:231], v[116:119], v[0:15]
	v_add_f32_e32 v254, v173, v254
	v_add_f32_e32 v213, v254, v213
	s_cbranch_vccnz .LBB4_878
	v_med3_f32 v113, v160, -v255, v255
	v_med3_f32 v114, v164, -v255, v255
	v_cvt_scalef32_pk_fp8_f32 v115, v113, v114, s93
	v_med3_f32 v113, v161, -v255, v255
	v_med3_f32 v114, v165, -v255, v255
	v_cvt_scalef32_pk_fp8_f32 v116, v113, v114, s93
	v_med3_f32 v113, v162, -v255, v255
	v_med3_f32 v114, v166, -v255, v255
	s_bitcmp1_b32 s58, 0
	v_cvt_scalef32_pk_fp8_f32 v117, v113, v114, s93
	s_cselect_b32 s8, 0x1100, 0
	v_med3_f32 v113, v163, -v255, v255
	v_med3_f32 v114, v167, -v255, v255
	v_cmp_eq_u32_e32 vcc, 0, v181
	v_add_u32_e32 v112, s8, v190
	v_cvt_scalef32_pk_fp8_f32 v118, v113, v114, s93
	s_and_b64 vcc, exec, vcc
	s_and_b32 s34, s58, 31
	ds_write_b16 v112, v115
	ds_write_b16 v112, v116 offset:68
	ds_write_b16 v112, v117 offset:136
	ds_write_b16 v112, v118 offset:204
	s_cbranch_vccnz .LBB4_883
	s_lshl_b32 s8, s34, 7
	s_lshl_b32 s9, s58, 6
	s_and_b32 s8, s8, 0xf00
	s_and_b32 s9, s9, 64
	s_or_b32 s26, s8, s9
	s_cbranch_execnz .LBB4_877

; DI void finishSM(f32x16& p0, f32x16& p1, float alpha, float& l_reg, bf16x8& pa0, bf16x8& pa1, bf16x8& pa2, bf16x8& pa3) {
; #pragma unroll
;     for (int r = 0; r < 16; ++r) p1[r] = __builtin_amdgcn_exp2f(p1[r]);
;     float ps = 0;
; #pragma unroll
;     for (int r = 0; r < 16; ++r) ps += p0[r];
; #pragma unroll
;     for (int r = 0; r < 16; ++r) ps += p1[r];
;     { auto rr = __builtin_amdgcn_permlane32_swap(__float_as_uint(ps), __float_as_uint(ps), false, false); ps = __uint_as_float(rr[0]) + __uint_as_float(rr[1]); }
;     l_reg = l_reg * alpha + ps;
;     ...
;     AT_PK4(p0, 0, pa0); AT_PK4(p0, 8, pa1); AT_PK4(p1, 0, pa2); AT_PK4(p1, 8, pa3);
;     ...
; }
; DI void qkt(f32x16& p0, f32x16& p1, const char* Ks, const bf16x8* qr, const f32x16& negm, int r32, int hi) {
; #pragma unroll
;     for (int d0 = 0; d0 < 4; ++d0) { const int cb = (d0 * 16 + hi * 8) * 2;
;         const bf16x8 b0 = *reinterpret_cast<const bf16x8*>(Ks + AT_KSWZ(r32, cb));
;         const bf16x8 b1 = *reinterpret_cast<const bf16x8*>(Ks + AT_KSWZ(32 + r32, cb));
;         p0 = __builtin_amdgcn_mfma_f32_32x32x16_bf16(b0, qr[d0], d0 == 0 ? negm : p0, 0, 0, 0);
;         p1 = __builtin_amdgcn_mfma_f32_32x32x16_bf16(b1, qr[d0], d0 == 0 ? negm : p1, 0, 0, 0); }
; }
.LBB4_923:
	s_lshl_b32 s18, s30, 13
	s_add_i32 s18, s18, 0
	v_add_u32_e32 v72, s18, v208
	v_add_u32_e32 v112, s18, v209
	v_add_u32_e32 v180, s18, v210
	s_waitcnt lgkmcnt(1)
	v_mfma_f32_32x32x16_bf16 v[128:143], v[64:67], v[156:159], v[80:95]
	ds_read_b128 v[64:67], v72 offset:49152
	ds_read_b128 v[72:75], v72 offset:53248
	ds_read_b128 v[76:79], v112 offset:49152
	ds_read_b128 v[224:227], v112 offset:53248
	v_exp_f32_e32 v182, v97
	v_exp_f32_e32 v217, v98
	v_exp_f32_e32 v218, v99
	v_exp_f32_e32 v223, v100
	v_exp_f32_e32 v232, v101
	s_waitcnt lgkmcnt(4)
	v_mfma_f32_32x32x16_bf16 v[112:127], v[68:71], v[156:159], v[80:95]
	ds_read_b128 v[68:71], v180 offset:49152
	ds_read_b128 v[228:231], v180 offset:53248
	v_exp_f32_e32 v180, v96
	v_cvt_pk_bf16_f32 v96, v220, v222
	v_cvt_pk_bf16_f32 v97, v179, v221
	v_cvt_pk_bf16_f32 v98, v177, v219
	v_cvt_pk_bf16_f32 v99, v176, v178
	s_waitcnt lgkmcnt(4)
	v_mfma_f32_32x32x16_bf16 v[112:127], v[72:75], v[152:155], v[112:127]
	v_add_f32_e32 v75, 0, v220
	v_add_f32_e32 v75, v222, v75
	v_add_f32_e32 v75, v221, v75
	v_add_f32_e32 v75, v219, v75
	v_add_f32_e32 v75, v176, v75
	v_mfma_f32_32x32x16_bf16 v[128:143], v[64:67], v[152:155], v[128:143]
	v_add_f32_e32 v75, v172, v75
	s_waitcnt lgkmcnt(3)
	v_mfma_f32_32x32x16_bf16 v[128:143], v[76:79], v[148:151], v[128:143]
	v_add_f32_e32 v75, v180, v75
	v_add_f32_e32 v75, v182, v75
	v_exp_f32_e32 v64, v102
	v_exp_f32_e32 v65, v103
	v_exp_f32_e32 v66, v104
	s_waitcnt lgkmcnt(2)
	v_mfma_f32_32x32x16_bf16 v[112:127], v[224:227], v[148:151], v[112:127]
	v_exp_f32_e32 v67, v105
	v_exp_f32_e32 v105, v106
	v_exp_f32_e32 v106, v107
	v_exp_f32_e32 v107, v108
	v_exp_f32_e32 v72, v109
	v_exp_f32_e32 v73, v110
	v_exp_f32_e32 v74, v111
	s_waitcnt lgkmcnt(1)
	v_mfma_f32_32x32x16_bf16 v[128:143], v[68:71], v[144:147], v[128:143]
	v_add_f32_e32 v68, v217, v75
	v_add_f32_e32 v68, v218, v68
	v_add_f32_e32 v68, v223, v68
	v_add_f32_e32 v68, v232, v68
	v_add_f32_e32 v68, v64, v68
	v_add_f32_e32 v68, v65, v68
	v_add_f32_e32 v68, v66, v68
	v_add_f32_e32 v68, v67, v68
	s_waitcnt lgkmcnt(0)
	v_mfma_f32_32x32x16_bf16 v[112:127], v[228:231], v[144:147], v[112:127]
	v_add_f32_e32 v68, v105, v68
	v_add_f32_e32 v68, v106, v68
	v_add_f32_e32 v68, v107, v68
	v_add_f32_e32 v68, v72, v68
	v_add_f32_e32 v68, v73, v68
	v_add_f32_e32 v215, v74, v68
	v_cvt_pk_bf16_f32 v108, v173, v175
	v_cvt_pk_bf16_f32 v109, v171, v174
	v_cvt_pk_bf16_f32 v110, v169, v172
	v_cvt_pk_bf16_f32 v111, v168, v170
	v_cvt_pk_bf16_f32 v100, v180, v182
	v_cvt_pk_bf16_f32 v101, v217, v218
	v_cvt_pk_bf16_f32 v102, v223, v232
	v_cvt_pk_bf16_f32 v103, v64, v65
	v_cvt_pk_bf16_f32 v104, v66, v67
	v_cvt_pk_bf16_f32 v105, v105, v106
	v_cvt_pk_bf16_f32 v106, v107, v72
	v_cvt_pk_bf16_f32 v107, v73, v74
	s_add_u32 s34, s46, s16
	s_addc_u32 s35, s47, s17
	s_add_u32 s24, s34, 0x23808000
	s_addc_u32 s25, s35, 0
	s_add_u32 s54, s34, 0x2380a000
	s_addc_u32 s55, s35, 0
	s_add_u32 s42, s46, s20
	s_addc_u32 s43, s47, s21
	s_add_u32 s56, s42, 0x21884000
	s_addc_u32 s57, s43, 0
	s_lshl_b32 s92, s15, 14
	s_add_i32 s92, s92, s94
	s_mov_b32 m0, s92
	s_lshl_b32 s96, s15, 13
	global_load_lds_dwordx4 v249, s[24:25]
	s_addk_i32 s92, 0x400
	s_mov_b32 m0, s92
	s_add_i32 s96, s96, s95
	global_load_lds_dwordx4 v250, s[24:25]
	s_nop 0
	s_mov_b32 m0, s96
	s_nop 0
	global_load_lds_dwordx4 v251, s[56:57]
	s_andn2_b64 vcc, exec, s[2:3]
	s_cbranch_vccnz .LBB4_925
	s_mov_b64 s[2:3], s[8:9]
	global_store_dwordx2 v193, v[184:185], s[2:3] nt

; #define AT_SBAR() __builtin_amdgcn_sched_barrier(0)
; template <int OFF> DI s16x4 tr_read(int vb) { s16x4 r; asm volatile("ds_read_b64_tr_b16 %0, %1 offset:%2" : "=&v"(r) : "v"(vb), "i"(OFF) : "memory"); return r; }
; template <int D0> DI void pv_one(f32x16& od, int vb, bf16x8 pa0, bf16x8 pa1, bf16x8 pa2, bf16x8 pa3) {
;     const s16x4 l0 = tr_read<v_rd_off(D0, 0, 0)>(vb), h0 = tr_read<v_rd_off(D0, 0, 1)>(vb), l1 = tr_read<v_rd_off(D0, 1, 0)>(vb), h1 = tr_read<v_rd_off(D0, 1, 1)>(vb);
;     const s16x4 l2 = tr_read<v_rd_off(D0, 2, 0)>(vb), h2 = tr_read<v_rd_off(D0, 2, 1)>(vb), l3 = tr_read<v_rd_off(D0, 3, 0)>(vb), h3 = tr_read<v_rd_off(D0, 3, 1)>(vb);
;     asm volatile("s_waitcnt lgkmcnt(0)" ::: "memory"); AT_SBAR();
;     ...
;     od = __builtin_amdgcn_mfma_f32_32x32x16_bf16(AT_PK(l0, h0), pa0, od, 0, 0, 0);
;     od = __builtin_amdgcn_mfma_f32_32x32x16_bf16(AT_PK(l1, h1), pa1, od, 0, 0, 0);
;     od = __builtin_amdgcn_mfma_f32_32x32x16_bf16(AT_PK(l2, h2), pa2, od, 0, 0, 0);
;     od = __builtin_amdgcn_mfma_f32_32x32x16_bf16(AT_PK(l3, h3), pa3, od, 0, 0, 0);
;     ...
; }
.LBB4_927:
	ds_read_b64_tr_b16 v[218:219], v182 offset:0x600
	ds_read_b64_tr_b16 v[220:221], v182 offset:0x700
	ds_read_b64_tr_b16 v[222:223], v182 offset:0x1600
	ds_read_b64_tr_b16 v[224:225], v182 offset:0x1700
	ds_read_b64_tr_b16 v[226:227], v182 offset:0x2600
	ds_read_b64_tr_b16 v[228:229], v182 offset:0x2700
	ds_read_b64_tr_b16 v[230:231], v182 offset:0x3600
	ds_read_b64_tr_b16 v[232:233], v182 offset:0x3700
	s_waitcnt lgkmcnt(0)
	v_mfma_f32_32x32x16_bf16 v[0:15], v[218:221], v[96:99], v[0:15]
	s_lshl_b32 s2, s15, 14
	s_lshl_b32 s3, s15, 13
	s_sub_i32 s54, s2, s3
	s_waitcnt vmcnt(3)
	v_mfma_f32_32x32x16_bf16 v[0:15], v[222:225], v[108:111], v[0:15]
	s_andn2_b64 s[2:3], exec, s[22:23]
	s_andn2_b64 vcc, exec, s[22:23]
	v_mfma_f32_32x32x16_bf16 v[0:15], v[226:229], v[100:103], v[0:15]
	v_mfma_f32_32x32x16_bf16 v[0:15], v[230:233], v[104:107], v[0:15]
	v_add_f32_e32 v254, v170, v254
	v_add_f32_e32 v215, v254, v215
	s_cbranch_vccnz .LBB4_932
	v_med3_f32 v97, v160, -v255, v255
	v_med3_f32 v98, v164, -v255, v255
	v_cvt_scalef32_pk_fp8_f32 v99, v97, v98, s93
	v_med3_f32 v97, v161, -v255, v255
	v_med3_f32 v98, v165, -v255, v255
	v_cvt_scalef32_pk_fp8_f32 v100, v97, v98, s93
	v_med3_f32 v97, v162, -v255, v255
	v_med3_f32 v98, v166, -v255, v255
	s_bitcmp1_b32 s58, 0
	v_cvt_scalef32_pk_fp8_f32 v101, v97, v98, s93
	s_cselect_b32 s8, 0x1100, 0
	v_med3_f32 v97, v163, -v255, v255
	v_med3_f32 v98, v167, -v255, v255
	v_cmp_eq_u32_e32 vcc, 0, v181
	v_add_u32_e32 v96, s8, v195
	v_cvt_scalef32_pk_fp8_f32 v102, v97, v98, s93
	s_and_b64 vcc, exec, vcc
	s_and_b32 s22, s58, 31
	ds_write_b16 v96, v99
	ds_write_b16 v96, v100 offset:68
	ds_write_b16 v96, v101 offset:136
	ds_write_b16 v96, v102 offset:204
	s_cbranch_vccnz .LBB4_956
	s_lshl_b32 s8, s22, 7
	s_lshl_b32 s9, s58, 6
	s_and_b32 s8, s8, 0xf00
	s_and_b32 s9, s9, 64
	s_or_b32 s18, s8, s9
	s_cbranch_execnz .LBB4_931

; DI void finishSM(f32x16& p0, f32x16& p1, float alpha, float& l_reg, bf16x8& pa0, bf16x8& pa1, bf16x8& pa2, bf16x8& pa3) {
; #pragma unroll
;     for (int r = 0; r < 16; ++r) p1[r] = __builtin_amdgcn_exp2f(p1[r]);
;     float ps = 0;
; #pragma unroll
;     for (int r = 0; r < 16; ++r) ps += p0[r];
; #pragma unroll
;     for (int r = 0; r < 16; ++r) ps += p1[r];
;     { auto rr = __builtin_amdgcn_permlane32_swap(__float_as_uint(ps), __float_as_uint(ps), false, false); ps = __uint_as_float(rr[0]) + __uint_as_float(rr[1]); }
;     l_reg = l_reg * alpha + ps;
;     ...
;     AT_PK4(p0, 0, pa0); AT_PK4(p0, 8, pa1); AT_PK4(p1, 0, pa2); AT_PK4(p1, 8, pa3);
;     ...
; }
; DI void qkt(f32x16& p0, f32x16& p1, const char* Ks, const bf16x8* qr, const f32x16& negm, int r32, int hi) {
; #pragma unroll
;     for (int d0 = 0; d0 < 4; ++d0) { const int cb = (d0 * 16 + hi * 8) * 2;
;         const bf16x8 b0 = *reinterpret_cast<const bf16x8*>(Ks + AT_KSWZ(r32, cb));
;         const bf16x8 b1 = *reinterpret_cast<const bf16x8*>(Ks + AT_KSWZ(32 + r32, cb));
;         p0 = __builtin_amdgcn_mfma_f32_32x32x16_bf16(b0, qr[d0], d0 == 0 ? negm : p0, 0, 0, 0);
;         p1 = __builtin_amdgcn_mfma_f32_32x32x16_bf16(b1, qr[d0], d0 == 0 ? negm : p1, 0, 0, 0); }
; }
.LBB4_944:
	v_exp_f32_e32 v182, v128
	v_exp_f32_e32 v234, v129
	v_exp_f32_e32 v235, v130
	v_exp_f32_e32 v236, v131
	v_exp_f32_e32 v237, v132
	v_exp_f32_e32 v238, v133
	v_exp_f32_e32 v239, v134
	v_exp_f32_e32 v240, v135
	v_exp_f32_e32 v241, v136
	v_exp_f32_e32 v242, v137
	v_exp_f32_e32 v243, v138
	v_exp_f32_e32 v244, v139
	v_exp_f32_e32 v245, v140
	v_exp_f32_e32 v246, v141
	v_exp_f32_e32 v247, v142
	v_exp_f32_e32 v248, v143
	v_add_u32_e32 v101, s54, v208
	v_add_u32_e32 v102, s54, v209
	v_add_u32_e32 v103, s54, v210
	ds_read_b128 v[172:175], v101 offset:49152
	ds_read_b128 v[176:179], v101 offset:53248
	ds_read_b128 v[218:221], v102 offset:49152
	ds_read_b128 v[222:225], v102 offset:53248
	ds_read_b128 v[226:229], v103 offset:49152
	ds_read_b128 v[230:233], v103 offset:53248
	v_exp_f32_e32 v112, v112
	v_exp_f32_e32 v113, v113
	v_exp_f32_e32 v114, v114
	s_waitcnt lgkmcnt(7)
	v_mfma_f32_32x32x16_bf16 v[128:143], v[96:99], v[156:159], v[80:95]
	v_exp_f32_e32 v115, v115
	v_exp_f32_e32 v116, v116
	v_exp_f32_e32 v117, v117
	v_exp_f32_e32 v118, v118
	v_exp_f32_e32 v119, v119
	s_waitcnt lgkmcnt(6)
	v_mfma_f32_32x32x16_bf16 v[96:111], v[168:171], v[156:159], v[80:95]
	v_exp_f32_e32 v168, v120
	v_add_f32_e32 v120, 0, v182
	v_add_f32_e32 v120, v234, v120
	v_add_f32_e32 v120, v235, v120
	v_add_f32_e32 v120, v236, v120
	v_add_f32_e32 v120, v237, v120
	v_add_f32_e32 v120, v238, v120
	v_add_f32_e32 v120, v239, v120
	v_add_f32_e32 v120, v240, v120
	v_add_f32_e32 v120, v241, v120
	v_add_f32_e32 v120, v242, v120
	s_waitcnt lgkmcnt(5)
	v_mfma_f32_32x32x16_bf16 v[128:143], v[172:175], v[152:155], v[128:143]
	v_add_f32_e32 v120, v243, v120
	v_add_f32_e32 v120, v244, v120
	v_add_f32_e32 v120, v245, v120
	v_add_f32_e32 v120, v246, v120
	v_add_f32_e32 v120, v247, v120
	v_add_f32_e32 v120, v248, v120
	v_add_f32_e32 v120, v112, v120
	s_waitcnt lgkmcnt(4)
	v_mfma_f32_32x32x16_bf16 v[96:111], v[176:179], v[152:155], v[96:111]
	v_add_f32_e32 v120, v113, v120
	v_add_f32_e32 v120, v114, v120
	v_add_f32_e32 v120, v115, v120
	v_add_f32_e32 v120, v116, v120
	v_exp_f32_e32 v169, v121
	v_add_f32_e32 v120, v117, v120
	v_exp_f32_e32 v170, v122
	s_waitcnt lgkmcnt(3)
	v_mfma_f32_32x32x16_bf16 v[128:143], v[218:221], v[148:151], v[128:143]
	v_add_f32_e32 v120, v118, v120
	v_exp_f32_e32 v171, v123
	v_add_f32_e32 v120, v119, v120
	v_exp_f32_e32 v172, v124
	v_exp_f32_e32 v173, v125
	s_waitcnt lgkmcnt(2)
	v_mfma_f32_32x32x16_bf16 v[96:111], v[222:225], v[148:151], v[96:111]
	v_exp_f32_e32 v174, v126
	v_exp_f32_e32 v175, v127
	v_add_f32_e32 v120, v174, v120
	s_waitcnt lgkmcnt(1)
	v_mfma_f32_32x32x16_bf16 v[128:143], v[226:229], v[144:147], v[128:143]
	v_add_f32_e32 v217, v175, v120
	v_cvt_pk_bf16_f32 v120, v182, v234
	v_cvt_pk_bf16_f32 v121, v235, v236
	v_cvt_pk_bf16_f32 v122, v237, v238
	v_cvt_pk_bf16_f32 v123, v239, v240
	v_cvt_pk_bf16_f32 v124, v241, v242
	s_waitcnt lgkmcnt(0)
	v_mfma_f32_32x32x16_bf16 v[96:111], v[230:233], v[144:147], v[96:111]
	v_cvt_pk_bf16_f32 v125, v243, v244
	v_cvt_pk_bf16_f32 v126, v245, v246
	v_cvt_pk_bf16_f32 v127, v247, v248
	v_cvt_pk_bf16_f32 v112, v112, v113
	v_cvt_pk_bf16_f32 v113, v114, v115
	v_cvt_pk_bf16_f32 v114, v116, v117
	v_cvt_pk_bf16_f32 v115, v118, v119
	v_cvt_pk_bf16_f32 v116, v168, v169
	v_cvt_pk_bf16_f32 v117, v170, v171
	v_cvt_pk_bf16_f32 v118, v172, v173
	v_cvt_pk_bf16_f32 v119, v174, v175
	s_add_u32 s24, s34, 0x2380c000
	s_addc_u32 s25, s35, 0
	s_add_u32 s34, s34, 0x2380e000
	s_addc_u32 s35, s35, 0
	s_add_u32 s42, s42, 0x21886000
	s_addc_u32 s43, s43, 0
	s_lshl_b32 s92, s29, 14
	s_add_i32 s92, s92, s94
	s_mov_b32 m0, s92
	s_lshl_b32 s96, s29, 13
	global_load_lds_dwordx4 v249, s[24:25]
	s_addk_i32 s92, 0x400
	s_mov_b32 m0, s92
	s_add_i32 s96, s96, s95
	global_load_lds_dwordx4 v250, s[24:25]
	s_nop 0
	s_mov_b32 m0, s96
	s_nop 0
	global_load_lds_dwordx4 v251, s[42:43]
	s_nop 0
	s_and_b64 vcc, exec, s[2:3]
	s_cbranch_vccnz .LBB4_946
	s_mov_b64 s[2:3], s[8:9]
	global_store_dwordx2 v193, v[184:185], s[2:3] nt

; #define AT_SBAR() __builtin_amdgcn_sched_barrier(0)
; template <int OFF> DI s16x4 tr_read(int vb) { s16x4 r; asm volatile("ds_read_b64_tr_b16 %0, %1 offset:%2" : "=&v"(r) : "v"(vb), "i"(OFF) : "memory"); return r; }
; template <int D0> DI void pv_one(f32x16& od, int vb, bf16x8 pa0, bf16x8 pa1, bf16x8 pa2, bf16x8 pa3) {
;     const s16x4 l0 = tr_read<v_rd_off(D0, 0, 0)>(vb), h0 = tr_read<v_rd_off(D0, 0, 1)>(vb), l1 = tr_read<v_rd_off(D0, 1, 0)>(vb), h1 = tr_read<v_rd_off(D0, 1, 1)>(vb);
;     const s16x4 l2 = tr_read<v_rd_off(D0, 2, 0)>(vb), h2 = tr_read<v_rd_off(D0, 2, 1)>(vb), l3 = tr_read<v_rd_off(D0, 3, 0)>(vb), h3 = tr_read<v_rd_off(D0, 3, 1)>(vb);
;     asm volatile("s_waitcnt lgkmcnt(0)" ::: "memory"); AT_SBAR();
;     ...
;     od = __builtin_amdgcn_mfma_f32_32x32x16_bf16(AT_PK(l0, h0), pa0, od, 0, 0, 0);
;     od = __builtin_amdgcn_mfma_f32_32x32x16_bf16(AT_PK(l1, h1), pa1, od, 0, 0, 0);
;     od = __builtin_amdgcn_mfma_f32_32x32x16_bf16(AT_PK(l2, h2), pa2, od, 0, 0, 0);
;     od = __builtin_amdgcn_mfma_f32_32x32x16_bf16(AT_PK(l3, h3), pa3, od, 0, 0, 0);
;     ...
; }
.LBB4_947:
	ds_read_b64_tr_b16 v[220:221], v219 offset:0x600
	ds_read_b64_tr_b16 v[222:223], v219 offset:0x700
	ds_read_b64_tr_b16 v[224:225], v219 offset:0x1600
	ds_read_b64_tr_b16 v[226:227], v219 offset:0x1700
	ds_read_b64_tr_b16 v[228:229], v219 offset:0x2600
	ds_read_b64_tr_b16 v[230:231], v219 offset:0x2700
	ds_read_b64_tr_b16 v[232:233], v219 offset:0x3600
	ds_read_b64_tr_b16 v[234:235], v219 offset:0x3700
	s_waitcnt lgkmcnt(0)
	v_mfma_f32_32x32x16_bf16 v[0:15], v[220:223], v[120:123], v[0:15]
	s_add_i32 s2, s31, 0
	s_waitcnt vmcnt(3)
	s_mov_b32 s18, 0
	s_andn2_b64 vcc, exec, s[22:23]
	v_mfma_f32_32x32x16_bf16 v[0:15], v[224:227], v[124:127], v[0:15]
	v_mfma_f32_32x32x16_bf16 v[0:15], v[228:231], v[112:115], v[0:15]
	s_andn2_b64 s[2:3], exec, s[22:23]
	v_mfma_f32_32x32x16_bf16 v[0:15], v[232:235], v[116:119], v[0:15]
	v_add_f32_e32 v254, v173, v254
	v_add_f32_e32 v217, v254, v217
	s_cbranch_vccnz .LBB4_952
	v_med3_f32 v113, v160, -v255, v255
	v_med3_f32 v114, v164, -v255, v255
	v_cvt_scalef32_pk_fp8_f32 v115, v113, v114, s93
	v_med3_f32 v113, v161, -v255, v255
	v_med3_f32 v114, v165, -v255, v255
	v_cvt_scalef32_pk_fp8_f32 v116, v113, v114, s93
	v_med3_f32 v113, v162, -v255, v255
	v_med3_f32 v114, v166, -v255, v255
	s_bitcmp1_b32 s58, 0
	v_cvt_scalef32_pk_fp8_f32 v117, v113, v114, s93
	s_cselect_b32 s8, 0x1100, 0
	v_med3_f32 v113, v163, -v255, v255
	v_med3_f32 v114, v167, -v255, v255
	v_cmp_eq_u32_e32 vcc, 0, v181
	v_add_u32_e32 v112, s8, v195
	v_cvt_scalef32_pk_fp8_f32 v118, v113, v114, s93
	s_and_b64 vcc, exec, vcc
	s_and_b32 s24, s58, 31
	ds_write_b16 v112, v115
	ds_write_b16 v112, v116 offset:68
	ds_write_b16 v112, v117 offset:136
	ds_write_b16 v112, v118 offset:204
	s_cbranch_vccnz .LBB4_957
	s_lshl_b32 s8, s24, 7
	s_lshl_b32 s9, s58, 6
	s_and_b32 s8, s8, 0xf00
	s_and_b32 s9, s9, 64
	s_or_b32 s18, s8, s9
	s_cbranch_execnz .LBB4_951
